# v38 with P4 epilogue software-pipelined: all 4 gate loads of a 16-row block issued two blocks ahead into 3 rotating register sets, counted vmcnt waits
# speedup vs baseline: 1.0010x; 1.0010x over previous
; #define LAS __attribute__((address_space(3)))
; __device__ __forceinline__ unsigned pk4_fp8(float a, float b, float c, float d) { int w = 0; w = __builtin_amdgcn_cvt_pk_fp8_f32(a, b, w, false); w = __builtin_amdgcn_cvt_pk_fp8_f32(c, d, w, true); return (unsigned)w; }
; __device__ __forceinline__ float bf_lo(unsigned w) { return __uint_as_float(w << 16); }
; __device__ __forceinline__ float bf_hi(unsigned w) { return __uint_as_float(w & 0xffff0000u); }
; __device__ __forceinline__ float sigmoidf_fast(float x) { return __builtin_amdgcn_rcpf(1.0f + __builtin_amdgcn_exp2f(-1.4426950408889634f * x)); }
;     __device__ __forceinline__ void operator()(f32x4 (&acc)[2][2][4][2], const Unit& u, int wr, int wc, int fr, int fq) const {
;     ...
;                 const size_t ro = (size_t)(u.row0 + ai * 128 + wr * 64 + m * 16 + fr) * DM + col0;
; #pragma unroll
;                 for (int bj = 0; bj < 2; ++bj) {
;                     const u32x4 gd = *(const u32x4*)(GDF + ro + bj * 32);
;                     const float ed[8] = {bf_lo(gd.x), bf_hi(gd.x), bf_lo(gd.y), bf_hi(gd.y), bf_lo(gd.z), bf_hi(gd.z), bf_lo(gd.w), bf_hi(gd.w)};
;                     if (u.tag == 0) {
;                         const u32x4 gn = *(const u32x4*)(GNA + ro + bj * 32);
;                         const float en[8] = {bf_lo(gn.x), bf_hi(gn.x), bf_lo(gn.y), bf_hi(gn.y), bf_lo(gn.z), bf_hi(gn.z), bf_lo(gn.w), bf_hi(gn.w)};
; #pragma unroll
;                         for (int e = 0; e < 8; ++e) {
;                             const float r = (1.0f + __builtin_amdgcn_exp2f(-1.4426950408889634f * ed[e])) * __builtin_amdgcn_rcpf(1.0f + __builtin_amdgcn_exp2f(-1.4426950408889634f * en[e]));
;                             acc[ai][bj][m][e >> 2][e & 3] *= r; }
;                     } else {
;                         float y[8];
; #pragma unroll
;                         for (int e = 0; e < 8; ++e) y[e] = acc[ai][bj][m][e >> 2][e & 3] * sigmoidf_fast(ed[e]) * (PSCALE * WSCALE_INV * OSCALE_INV);
;                         u32x2 w; w.x = pk4_fp8(y[0], y[1], y[2], y[3]); w.y = pk4_fp8(y[4], y[5], y[6], y[7]);
;                         *(LAS u32x2*)(my + fr * 80 + bj * 32 + fq * 8) = w;
;                     }
.LBB0_561:
	s_nop 15
	s_nop 15
	v_add_u32_e32 v4, s76, v164
	v_add_u32_e32 v2, s54, v167
	v_ashrrev_i32_e32 v5, 31, v4
	v_ashrrev_i32_e32 v3, 31, v2
	v_lshlrev_b64 v[6:7], 11, v[4:5]
	v_lshl_add_u64 v[8:9], v[6:7], 0, v[2:3]
	v_lshl_add_u64 v[6:7], v[8:9], 1, s[40:41]
	v_add_u32_e32 v248, s76, v164
	v_ashrrev_i32_e32 v249, 31, v248
	v_lshlrev_b64 v[248:249], 11, v[248:249]
	v_lshl_add_u64 v[248:249], v[248:249], 0, v[2:3]
	v_lshl_add_u64 v[250:251], v[248:249], 1, s[40:41]
	global_load_dwordx4 v[194:197], v[250:251], off nt
	global_load_dwordx4 v[198:201], v[250:251], off offset:64 nt
	v_lshl_add_u64 v[250:251], v[248:249], 1, s[38:39]
	global_load_dwordx4 v[202:205], v[250:251], off nt
	global_load_dwordx4 v[206:209], v[250:251], off offset:64 nt
	v_add_u32_e32 v248, s76, v168
	v_ashrrev_i32_e32 v249, 31, v248
	v_lshlrev_b64 v[248:249], 11, v[248:249]
	v_lshl_add_u64 v[248:249], v[248:249], 0, v[2:3]
	v_lshl_add_u64 v[250:251], v[248:249], 1, s[40:41]
	global_load_dwordx4 v[210:213], v[250:251], off nt
	global_load_dwordx4 v[214:217], v[250:251], off offset:64 nt
	v_lshl_add_u64 v[250:251], v[248:249], 1, s[38:39]
	global_load_dwordx4 v[218:221], v[250:251], off nt
	global_load_dwordx4 v[222:225], v[250:251], off offset:64 nt
	v_add_u32_e32 v248, s76, v171
	v_ashrrev_i32_e32 v249, 31, v248
	v_lshlrev_b64 v[248:249], 11, v[248:249]
	v_lshl_add_u64 v[248:249], v[248:249], 0, v[2:3]
	v_lshl_add_u64 v[250:251], v[248:249], 1, s[40:41]
	global_load_dwordx4 v[226:229], v[250:251], off nt
	global_load_dwordx4 v[230:233], v[250:251], off offset:64 nt
	v_lshl_add_u64 v[250:251], v[248:249], 1, s[38:39]
	global_load_dwordx4 v[234:237], v[250:251], off nt
	global_load_dwordx4 v[238:241], v[250:251], off offset:64 nt
	v_cndmask_b32_e64 v5, 0, 1, s[58:59]
	v_cmp_ne_u32_e64 s[4:5], 1, v5
	s_andn2_b64 vcc, exec, s[58:59]
	s_mov_b64 s[58:59], -1
	s_waitcnt vmcnt(8)
	v_mov_b64_e32 v[156:157], v[194:195]
	v_mov_b64_e32 v[158:159], v[196:197]
	v_lshlrev_b32_e32 v160, 16, v156
	v_and_b32_e32 v156, 0xffff0000, v156
	v_lshlrev_b32_e32 v161, 16, v157
	v_and_b32_e32 v157, 0xffff0000, v157
	v_lshlrev_b32_e32 v162, 16, v158
	v_and_b32_e32 v158, 0xffff0000, v158
	v_lshlrev_b32_e32 v163, 16, v159
	v_and_b32_e32 v159, 0xffff0000, v159
	v_mul_f32_e32 v160, 0xbfb8aa3b, v160
	v_mul_f32_e32 v156, 0xbfb8aa3b, v156
	v_mul_f32_e32 v181, 0xbfb8aa3b, v161
	v_mul_f32_e32 v157, 0xbfb8aa3b, v157
	v_mul_f32_e32 v182, 0xbfb8aa3b, v162
	v_mul_f32_e32 v158, 0xbfb8aa3b, v158
	v_mul_f32_e32 v183, 0xbfb8aa3b, v163
	v_mul_f32_e32 v159, 0xbfb8aa3b, v159
	v_exp_f32_e32 v160, v160
	v_exp_f32_e32 v161, v156
	v_exp_f32_e32 v162, v181
	v_exp_f32_e32 v163, v157
	v_exp_f32_e32 v156, v182
	v_exp_f32_e32 v157, v158
	v_exp_f32_e32 v158, v183
	v_exp_f32_e32 v159, v159
	s_cbranch_vccnz .LBB0_563
	v_add_f32_e32 v182, 1.0, v162
	v_rcp_f32_e32 v182, v182
	v_add_f32_e32 v183, 1.0, v163
	v_rcp_f32_e32 v183, v183
	v_add_f32_e32 v184, 1.0, v156
	v_rcp_f32_e32 v184, v184
	v_mul_f32_e32 v182, v136, v182
	v_mul_f32_e32 v185, 0x3c000000, v182
	v_mul_f32_e32 v182, v137, v183
	v_add_f32_e32 v183, 1.0, v157
	v_mul_f32_e32 v186, 0x3c000000, v182
	v_mul_f32_e32 v182, v130, v184
	v_rcp_f32_e32 v183, v183
	v_add_f32_e32 v184, 1.0, v158
	v_rcp_f32_e32 v184, v184
	v_add_f32_e32 v5, 1.0, v160
	v_add_f32_e32 v181, 1.0, v161
	v_rcp_f32_e32 v5, v5
	v_rcp_f32_e32 v181, v181
	v_mul_f32_e32 v187, 0x3c000000, v182
	v_mul_f32_e32 v182, v131, v183
	v_mul_f32_e32 v188, 0x3c000000, v182
	v_mul_f32_e32 v182, v132, v184
	v_mul_f32_e32 v184, 0x3c000000, v182
	v_add_f32_e32 v182, 1.0, v159
	v_mul_f32_e32 v5, v134, v5
	v_mul_f32_e32 v181, v135, v181
	v_rcp_f32_e32 v189, v182
	v_mul_f32_e32 v5, 0x3c000000, v5
	v_mul_f32_e32 v181, 0x3c000000, v181
	v_mov_b32_e32 v182, 0
	v_mov_b32_e32 v183, 0
	v_cvt_pk_fp8_f32 v182, v5, v181
	v_cvt_pk_fp8_f32 v183, v187, v188
	v_mul_f32_e32 v5, v133, v189
	v_mul_f32_e32 v5, 0x3c000000, v5
	v_cvt_pk_fp8_f32 v182, v185, v186 op_sel:[0,0,1]
	v_cvt_pk_fp8_f32 v183, v184, v5 op_sel:[0,0,1]
	s_mov_b64 s[58:59], 0
	ds_write_b64 v180, v[182:183]
; #define LAS __attribute__((address_space(3)))
; __device__ __forceinline__ unsigned pk4_fp8(float a, float b, float c, float d) { int w = 0; w = __builtin_amdgcn_cvt_pk_fp8_f32(a, b, w, false); w = __builtin_amdgcn_cvt_pk_fp8_f32(c, d, w, true); return (unsigned)w; }
; __device__ __forceinline__ float bf_lo(unsigned w) { return __uint_as_float(w << 16); }
; __device__ __forceinline__ float bf_hi(unsigned w) { return __uint_as_float(w & 0xffff0000u); }
; __device__ __forceinline__ float sigmoidf_fast(float x) { return __builtin_amdgcn_rcpf(1.0f + __builtin_amdgcn_exp2f(-1.4426950408889634f * x)); }
;     __device__ __forceinline__ void operator()(f32x4 (&acc)[2][2][4][2], const Unit& u, int wr, int wc, int fr, int fq) const {
;     ...
;                     const u32x4 gd = *(const u32x4*)(GDF + ro + bj * 32);
;                     const float ed[8] = {bf_lo(gd.x), bf_hi(gd.x), bf_lo(gd.y), bf_hi(gd.y), bf_lo(gd.z), bf_hi(gd.z), bf_lo(gd.w), bf_hi(gd.w)};
;                     if (u.tag == 0) {
;                         const u32x4 gn = *(const u32x4*)(GNA + ro + bj * 32);
;                         const float en[8] = {bf_lo(gn.x), bf_hi(gn.x), bf_lo(gn.y), bf_hi(gn.y), bf_lo(gn.z), bf_hi(gn.z), bf_lo(gn.w), bf_hi(gn.w)};
; #pragma unroll
;                         for (int e = 0; e < 8; ++e) {
;                             const float r = (1.0f + __builtin_amdgcn_exp2f(-1.4426950408889634f * ed[e])) * __builtin_amdgcn_rcpf(1.0f + __builtin_amdgcn_exp2f(-1.4426950408889634f * en[e]));
;                             acc[ai][bj][m][e >> 2][e & 3] *= r; }
;                     } else {
;                         float y[8];
; #pragma unroll
;                         for (int e = 0; e < 8; ++e) y[e] = acc[ai][bj][m][e >> 2][e & 3] * sigmoidf_fast(ed[e]) * (PSCALE * WSCALE_INV * OSCALE_INV);
;                         u32x2 w; w.x = pk4_fp8(y[0], y[1], y[2], y[3]); w.y = pk4_fp8(y[4], y[5], y[6], y[7]);
;                         *(LAS u32x2*)(my + fr * 80 + bj * 32 + fq * 8) = w;
;                     }
.LBB0_563:
	s_andn2_b64 vcc, exec, s[58:59]
	v_lshl_add_u64 v[8:9], v[8:9], 1, s[38:39]
	s_cbranch_vccnz .LBB0_565
	v_pk_add_f32 v[162:163], v[162:163], 1.0 op_sel_hi:[1,0]
	v_pk_add_f32 v[160:161], v[160:161], 1.0 op_sel_hi:[1,0]
	v_pk_add_f32 v[158:159], v[158:159], 1.0 op_sel_hi:[1,0]
	v_pk_add_f32 v[156:157], v[156:157], 1.0 op_sel_hi:[1,0]
	s_waitcnt vmcnt(8)
	v_mov_b64_e32 v[182:183], v[202:203]
	v_mov_b64_e32 v[184:185], v[204:205]
	v_lshlrev_b32_e32 v5, 16, v182
	v_and_b32_e32 v181, 0xffff0000, v182
	v_lshlrev_b32_e32 v182, 16, v183
	v_and_b32_e32 v183, 0xffff0000, v183
	v_lshlrev_b32_e32 v186, 16, v184
	v_and_b32_e32 v184, 0xffff0000, v184
	v_lshlrev_b32_e32 v187, 16, v185
	v_and_b32_e32 v185, 0xffff0000, v185
	v_mul_f32_e32 v5, 0xbfb8aa3b, v5
	v_mul_f32_e32 v181, 0xbfb8aa3b, v181
	v_mul_f32_e32 v182, 0xbfb8aa3b, v182
	v_mul_f32_e32 v183, 0xbfb8aa3b, v183
	v_mul_f32_e32 v186, 0xbfb8aa3b, v186
	v_mul_f32_e32 v184, 0xbfb8aa3b, v184
	v_mul_f32_e32 v187, 0xbfb8aa3b, v187
	v_mul_f32_e32 v185, 0xbfb8aa3b, v185
	v_exp_f32_e32 v5, v5
	v_exp_f32_e32 v181, v181
	v_exp_f32_e32 v182, v182
	v_exp_f32_e32 v183, v183
	v_exp_f32_e32 v186, v186
	v_exp_f32_e32 v184, v184
	v_exp_f32_e32 v187, v187
	v_exp_f32_e32 v185, v185
	v_add_f32_e32 v5, 1.0, v5
	v_add_f32_e32 v181, 1.0, v181
	v_add_f32_e32 v188, 1.0, v182
	v_add_f32_e32 v189, 1.0, v183
	v_add_f32_e32 v186, 1.0, v186
	v_add_f32_e32 v190, 1.0, v184
	v_add_f32_e32 v191, 1.0, v187
	v_add_f32_e32 v192, 1.0, v185
	v_rcp_f32_e32 v182, v5
	v_rcp_f32_e32 v183, v181
	v_rcp_f32_e32 v184, v188
	v_rcp_f32_e32 v185, v189
	v_rcp_f32_e32 v186, v186
	v_rcp_f32_e32 v187, v190
	v_rcp_f32_e32 v188, v191
	v_rcp_f32_e32 v189, v192
	v_pk_mul_f32 v[160:161], v[160:161], v[182:183]
	v_pk_mul_f32 v[162:163], v[162:163], v[184:185]
	v_pk_mul_f32 v[156:157], v[156:157], v[186:187]
	v_pk_mul_f32 v[158:159], v[158:159], v[188:189]
	v_pk_mul_f32 v[136:137], v[136:137], v[162:163]
	v_pk_mul_f32 v[134:135], v[134:135], v[160:161]
	v_pk_mul_f32 v[132:133], v[132:133], v[158:159]
	v_pk_mul_f32 v[130:131], v[130:131], v[156:157]
.LBB0_565:
	s_and_b64 vcc, exec, s[4:5]
	s_mov_b64 s[58:59], -1
	s_waitcnt vmcnt(8)
	v_mov_b64_e32 v[156:157], v[198:199]
	v_mov_b64_e32 v[158:159], v[200:201]
	v_lshlrev_b32_e32 v5, 16, v156
	v_and_b32_e32 v6, 0xffff0000, v156
	v_lshlrev_b32_e32 v7, 16, v157
	v_and_b32_e32 v156, 0xffff0000, v157
	v_lshlrev_b32_e32 v157, 16, v158
	v_and_b32_e32 v158, 0xffff0000, v158
	v_lshlrev_b32_e32 v160, 16, v159
	v_and_b32_e32 v159, 0xffff0000, v159
	v_mul_f32_e32 v5, 0xbfb8aa3b, v5
	v_mul_f32_e32 v6, 0xbfb8aa3b, v6
	v_mul_f32_e32 v7, 0xbfb8aa3b, v7
	v_mul_f32_e32 v156, 0xbfb8aa3b, v156
	v_mul_f32_e32 v157, 0xbfb8aa3b, v157
	v_mul_f32_e32 v162, 0xbfb8aa3b, v158
	v_mul_f32_e32 v163, 0xbfb8aa3b, v160
	v_mul_f32_e32 v181, 0xbfb8aa3b, v159
	v_exp_f32_e32 v158, v5
	v_exp_f32_e32 v159, v6
	v_exp_f32_e32 v160, v7
	v_exp_f32_e32 v161, v156
	v_exp_f32_e32 v6, v157
	v_exp_f32_e32 v7, v162
	v_exp_f32_e32 v156, v163
	v_exp_f32_e32 v157, v181
	s_cbranch_vccnz .LBB0_624
	v_add_f32_e32 v162, 1.0, v159
	v_add_f32_e32 v163, 1.0, v160
	v_rcp_f32_e32 v162, v162
	v_rcp_f32_e32 v163, v163
	v_add_f32_e32 v182, 1.0, v6
	v_rcp_f32_e32 v182, v182
	v_mul_f32_e32 v162, v103, v162
	v_mul_f32_e32 v181, 0x3c000000, v162
	v_mul_f32_e32 v162, v104, v163
	v_add_f32_e32 v163, 1.0, v161
	v_rcp_f32_e32 v163, v163
	v_mul_f32_e32 v183, 0x3c000000, v162
	v_add_f32_e32 v5, 1.0, v158
	v_rcp_f32_e32 v5, v5
	v_mul_f32_e32 v162, v105, v163
	v_add_f32_e32 v163, 1.0, v7
	v_mul_f32_e32 v184, 0x3c000000, v162
	v_mul_f32_e32 v162, v98, v182
	v_rcp_f32_e32 v163, v163
	v_add_f32_e32 v182, 1.0, v156
	v_rcp_f32_e32 v182, v182
	v_mul_f32_e32 v185, 0x3c000000, v162
	v_mul_f32_e32 v162, v99, v163
	v_mul_f32_e32 v186, 0x3c000000, v162
	v_mul_f32_e32 v162, v100, v182
	v_mul_f32_e32 v182, 0x3c000000, v162
	v_add_f32_e32 v162, 1.0, v157
	v_mul_f32_e32 v5, v102, v5
	v_rcp_f32_e32 v187, v162
	v_mul_f32_e32 v5, 0x3c000000, v5
	v_mov_b32_e32 v162, 0
	v_mov_b32_e32 v163, 0
	v_cvt_pk_fp8_f32 v162, v5, v181
	v_cvt_pk_fp8_f32 v163, v185, v186
	v_mul_f32_e32 v5, v101, v187
	v_mul_f32_e32 v5, 0x3c000000, v5
	v_cvt_pk_fp8_f32 v162, v183, v184 op_sel:[0,0,1]
	v_cvt_pk_fp8_f32 v163, v182, v5 op_sel:[0,0,1]
	ds_write_b64 v180, v[162:163] offset:32
	s_cbranch_execz .LBB0_625

; __device__ __forceinline__ float bf_lo(unsigned w) { return __uint_as_float(w << 16); }
; __device__ __forceinline__ float bf_hi(unsigned w) { return __uint_as_float(w & 0xffff0000u); }
;     __device__ __forceinline__ void operator()(f32x4 (&acc)[2][2][4][2], const Unit& u, int wr, int wc, int fr, int fq) const {
;     ...
;                 const size_t ro = (size_t)(u.row0 + ai * 128 + wr * 64 + m * 16 + fr) * DM + col0;
; #pragma unroll
;                 for (int bj = 0; bj < 2; ++bj) {
;                     const u32x4 gd = *(const u32x4*)(GDF + ro + bj * 32);
;                     const float ed[8] = {bf_lo(gd.x), bf_hi(gd.x), bf_lo(gd.y), bf_hi(gd.y), bf_lo(gd.z), bf_hi(gd.z), bf_lo(gd.w), bf_hi(gd.w)};
;                     if (u.tag == 0) {
;                         const u32x4 gn = *(const u32x4*)(GNA + ro + bj * 32);
;                         const float en[8] = {bf_lo(gn.x), bf_hi(gn.x), bf_lo(gn.y), bf_hi(gn.y), bf_lo(gn.z), bf_hi(gn.z), bf_lo(gn.w), bf_hi(gn.w)};
; #pragma unroll
;                         for (int e = 0; e < 8; ++e) {
;                             const float r = (1.0f + __builtin_amdgcn_exp2f(-1.4426950408889634f * ed[e])) * __builtin_amdgcn_rcpf(1.0f + __builtin_amdgcn_exp2f(-1.4426950408889634f * en[e]));
;                             acc[ai][bj][m][e >> 2][e & 3] *= r; }
.LBB0_569:
	s_nop 1
	v_add_u32_e32 v6, s76, v168
	v_ashrrev_i32_e32 v7, 31, v6
	v_lshlrev_b64 v[6:7], 11, v[6:7]
	v_lshl_add_u64 v[6:7], v[6:7], 0, v[2:3]
	v_lshl_add_u64 v[8:9], v[6:7], 1, s[40:41]
	v_add_u32_e32 v248, s76, v173
	v_ashrrev_i32_e32 v249, 31, v248
	v_lshlrev_b64 v[248:249], 11, v[248:249]
	v_lshl_add_u64 v[248:249], v[248:249], 0, v[2:3]
	v_lshl_add_u64 v[250:251], v[248:249], 1, s[40:41]
	global_load_dwordx4 v[194:197], v[250:251], off nt
	global_load_dwordx4 v[198:201], v[250:251], off offset:64 nt
	v_lshl_add_u64 v[250:251], v[248:249], 1, s[38:39]
	global_load_dwordx4 v[202:205], v[250:251], off nt
	global_load_dwordx4 v[206:209], v[250:251], off offset:64 nt
	s_and_b64 vcc, exec, s[4:5]
	s_mov_b64 s[58:59], -1
	s_waitcnt vmcnt(8)
	v_mov_b64_e32 v[156:157], v[210:211]
	v_mov_b64_e32 v[158:159], v[212:213]
	v_lshlrev_b32_e32 v5, 16, v156
	v_and_b32_e32 v156, 0xffff0000, v156
	v_lshlrev_b32_e32 v160, 16, v157
	v_and_b32_e32 v157, 0xffff0000, v157
	v_lshlrev_b32_e32 v161, 16, v158
	v_and_b32_e32 v158, 0xffff0000, v158
	v_lshlrev_b32_e32 v162, 16, v159
	v_and_b32_e32 v159, 0xffff0000, v159
	v_mul_f32_e32 v5, 0xbfb8aa3b, v5
	v_mul_f32_e32 v156, 0xbfb8aa3b, v156
	v_mul_f32_e32 v163, 0xbfb8aa3b, v160
	v_mul_f32_e32 v157, 0xbfb8aa3b, v157
	v_mul_f32_e32 v181, 0xbfb8aa3b, v161
	v_mul_f32_e32 v158, 0xbfb8aa3b, v158
	v_mul_f32_e32 v182, 0xbfb8aa3b, v162
	v_mul_f32_e32 v159, 0xbfb8aa3b, v159
	v_exp_f32_e32 v160, v5
	v_exp_f32_e32 v161, v156
	v_exp_f32_e32 v162, v163
	v_exp_f32_e32 v163, v157
	v_exp_f32_e32 v156, v181
	v_exp_f32_e32 v157, v158
	v_exp_f32_e32 v158, v182
	v_exp_f32_e32 v159, v159
	s_cbranch_vccnz .LBB0_571
	v_add_f32_e32 v182, 1.0, v162
	v_rcp_f32_e32 v182, v182
	v_add_f32_e32 v183, 1.0, v163
	v_rcp_f32_e32 v183, v183
	v_add_f32_e32 v184, 1.0, v156
	v_rcp_f32_e32 v184, v184
	v_mul_f32_e32 v182, v128, v182
	v_mul_f32_e32 v185, 0x3c000000, v182
	v_mul_f32_e32 v182, v129, v183
	v_add_f32_e32 v183, 1.0, v157
	v_mul_f32_e32 v186, 0x3c000000, v182
	v_mul_f32_e32 v182, v122, v184
	v_rcp_f32_e32 v183, v183
	v_add_f32_e32 v184, 1.0, v158
	v_rcp_f32_e32 v184, v184
	v_add_f32_e32 v5, 1.0, v160
	v_add_f32_e32 v181, 1.0, v161
	v_rcp_f32_e32 v5, v5
	v_rcp_f32_e32 v181, v181
	v_mul_f32_e32 v187, 0x3c000000, v182
	v_mul_f32_e32 v182, v123, v183
	v_mul_f32_e32 v188, 0x3c000000, v182
	v_mul_f32_e32 v182, v124, v184
	v_mul_f32_e32 v184, 0x3c000000, v182
	v_add_f32_e32 v182, 1.0, v159
	v_mul_f32_e32 v5, v126, v5
	v_mul_f32_e32 v181, v127, v181
	v_rcp_f32_e32 v189, v182
	v_mul_f32_e32 v5, 0x3c000000, v5
	v_mul_f32_e32 v181, 0x3c000000, v181
	v_mov_b32_e32 v182, 0
	v_mov_b32_e32 v183, 0
	v_cvt_pk_fp8_f32 v182, v5, v181
	v_cvt_pk_fp8_f32 v183, v187, v188
	v_mul_f32_e32 v5, v125, v189
	v_mul_f32_e32 v5, 0x3c000000, v5
	v_cvt_pk_fp8_f32 v182, v185, v186 op_sel:[0,0,1]
	v_cvt_pk_fp8_f32 v183, v184, v5 op_sel:[0,0,1]
	s_mov_b64 s[58:59], 0
	ds_write_b64 v180, v[182:183]
; #define LAS __attribute__((address_space(3)))
; __device__ __forceinline__ unsigned pk4_fp8(float a, float b, float c, float d) { int w = 0; w = __builtin_amdgcn_cvt_pk_fp8_f32(a, b, w, false); w = __builtin_amdgcn_cvt_pk_fp8_f32(c, d, w, true); return (unsigned)w; }
; __device__ __forceinline__ float bf_lo(unsigned w) { return __uint_as_float(w << 16); }
; __device__ __forceinline__ float bf_hi(unsigned w) { return __uint_as_float(w & 0xffff0000u); }
; __device__ __forceinline__ float sigmoidf_fast(float x) { return __builtin_amdgcn_rcpf(1.0f + __builtin_amdgcn_exp2f(-1.4426950408889634f * x)); }
;     __device__ __forceinline__ void operator()(f32x4 (&acc)[2][2][4][2], const Unit& u, int wr, int wc, int fr, int fq) const {
;     ...
;                 const size_t ro = (size_t)(u.row0 + ai * 128 + wr * 64 + m * 16 + fr) * DM + col0;
; #pragma unroll
;                 for (int bj = 0; bj < 2; ++bj) {
;                     const u32x4 gd = *(const u32x4*)(GDF + ro + bj * 32);
;                     const float ed[8] = {bf_lo(gd.x), bf_hi(gd.x), bf_lo(gd.y), bf_hi(gd.y), bf_lo(gd.z), bf_hi(gd.z), bf_lo(gd.w), bf_hi(gd.w)};
;                     if (u.tag == 0) {
;                         const u32x4 gn = *(const u32x4*)(GNA + ro + bj * 32);
;                         const float en[8] = {bf_lo(gn.x), bf_hi(gn.x), bf_lo(gn.y), bf_hi(gn.y), bf_lo(gn.z), bf_hi(gn.z), bf_lo(gn.w), bf_hi(gn.w)};
; #pragma unroll
;                         for (int e = 0; e < 8; ++e) {
;                             const float r = (1.0f + __builtin_amdgcn_exp2f(-1.4426950408889634f * ed[e])) * __builtin_amdgcn_rcpf(1.0f + __builtin_amdgcn_exp2f(-1.4426950408889634f * en[e]));
;                             acc[ai][bj][m][e >> 2][e & 3] *= r; }
;                     } else {
;                         float y[8];
; #pragma unroll
;                         for (int e = 0; e < 8; ++e) y[e] = acc[ai][bj][m][e >> 2][e & 3] * sigmoidf_fast(ed[e]) * (PSCALE * WSCALE_INV * OSCALE_INV);
;                         u32x2 w; w.x = pk4_fp8(y[0], y[1], y[2], y[3]); w.y = pk4_fp8(y[4], y[5], y[6], y[7]);
;                         *(LAS u32x2*)(my + fr * 80 + bj * 32 + fq * 8) = w;
.LBB0_571:
	s_andn2_b64 vcc, exec, s[58:59]
	v_lshl_add_u64 v[6:7], v[6:7], 1, s[38:39]
	s_cbranch_vccnz .LBB0_573
	v_pk_add_f32 v[162:163], v[162:163], 1.0 op_sel_hi:[1,0]
	v_pk_add_f32 v[160:161], v[160:161], 1.0 op_sel_hi:[1,0]
	v_pk_add_f32 v[158:159], v[158:159], 1.0 op_sel_hi:[1,0]
	v_pk_add_f32 v[156:157], v[156:157], 1.0 op_sel_hi:[1,0]
	s_waitcnt vmcnt(8)
	v_mov_b64_e32 v[182:183], v[218:219]
	v_mov_b64_e32 v[184:185], v[220:221]
	v_lshlrev_b32_e32 v5, 16, v182
	v_and_b32_e32 v181, 0xffff0000, v182
	v_lshlrev_b32_e32 v182, 16, v183
	v_and_b32_e32 v183, 0xffff0000, v183
	v_lshlrev_b32_e32 v186, 16, v184
	v_and_b32_e32 v184, 0xffff0000, v184
	v_lshlrev_b32_e32 v187, 16, v185
	v_and_b32_e32 v185, 0xffff0000, v185
	v_mul_f32_e32 v5, 0xbfb8aa3b, v5
	v_mul_f32_e32 v181, 0xbfb8aa3b, v181
	v_mul_f32_e32 v182, 0xbfb8aa3b, v182
	v_mul_f32_e32 v183, 0xbfb8aa3b, v183
	v_mul_f32_e32 v186, 0xbfb8aa3b, v186
	v_mul_f32_e32 v184, 0xbfb8aa3b, v184
	v_mul_f32_e32 v187, 0xbfb8aa3b, v187
	v_mul_f32_e32 v185, 0xbfb8aa3b, v185
	v_exp_f32_e32 v5, v5
	v_exp_f32_e32 v181, v181
	v_exp_f32_e32 v182, v182
	v_exp_f32_e32 v183, v183
	v_exp_f32_e32 v186, v186
	v_exp_f32_e32 v184, v184
	v_exp_f32_e32 v187, v187
	v_exp_f32_e32 v185, v185
	v_add_f32_e32 v5, 1.0, v5
	v_add_f32_e32 v181, 1.0, v181
	v_add_f32_e32 v188, 1.0, v182
	v_add_f32_e32 v189, 1.0, v183
	v_add_f32_e32 v186, 1.0, v186
	v_add_f32_e32 v190, 1.0, v184
	v_add_f32_e32 v191, 1.0, v187
	v_add_f32_e32 v192, 1.0, v185
	v_rcp_f32_e32 v182, v5
	v_rcp_f32_e32 v183, v181
	v_rcp_f32_e32 v184, v188
	v_rcp_f32_e32 v185, v189
	v_rcp_f32_e32 v186, v186
	v_rcp_f32_e32 v187, v190
	v_rcp_f32_e32 v188, v191
	v_rcp_f32_e32 v189, v192
	v_pk_mul_f32 v[160:161], v[160:161], v[182:183]
	v_pk_mul_f32 v[162:163], v[162:163], v[184:185]
	v_pk_mul_f32 v[156:157], v[156:157], v[186:187]
	v_pk_mul_f32 v[158:159], v[158:159], v[188:189]
	v_pk_mul_f32 v[128:129], v[128:129], v[162:163]
	v_pk_mul_f32 v[126:127], v[126:127], v[160:161]
	v_pk_mul_f32 v[124:125], v[124:125], v[158:159]
	v_pk_mul_f32 v[122:123], v[122:123], v[156:157]
.LBB0_573:
	s_and_b64 vcc, exec, s[4:5]
	s_mov_b64 s[58:59], -1
	s_waitcnt vmcnt(8)
	v_mov_b64_e32 v[156:157], v[214:215]
	v_mov_b64_e32 v[158:159], v[216:217]
	v_lshlrev_b32_e32 v5, 16, v156
	v_and_b32_e32 v8, 0xffff0000, v156
	v_lshlrev_b32_e32 v9, 16, v157
	v_and_b32_e32 v156, 0xffff0000, v157
	v_lshlrev_b32_e32 v157, 16, v158
	v_and_b32_e32 v158, 0xffff0000, v158
	v_lshlrev_b32_e32 v160, 16, v159
	v_and_b32_e32 v159, 0xffff0000, v159
	v_mul_f32_e32 v5, 0xbfb8aa3b, v5
	v_mul_f32_e32 v8, 0xbfb8aa3b, v8
	v_mul_f32_e32 v9, 0xbfb8aa3b, v9
	v_mul_f32_e32 v156, 0xbfb8aa3b, v156
	v_mul_f32_e32 v157, 0xbfb8aa3b, v157
	v_mul_f32_e32 v162, 0xbfb8aa3b, v158
	v_mul_f32_e32 v163, 0xbfb8aa3b, v160
	v_mul_f32_e32 v181, 0xbfb8aa3b, v159
	v_exp_f32_e32 v158, v5
	v_exp_f32_e32 v159, v8
	v_exp_f32_e32 v160, v9
	v_exp_f32_e32 v161, v156
	v_exp_f32_e32 v8, v157
	v_exp_f32_e32 v9, v162
	v_exp_f32_e32 v156, v163
	v_exp_f32_e32 v157, v181
	s_cbranch_vccnz .LBB0_626
	v_add_f32_e32 v162, 1.0, v159
	v_add_f32_e32 v163, 1.0, v160
	v_rcp_f32_e32 v162, v162
	v_rcp_f32_e32 v163, v163
	v_add_f32_e32 v182, 1.0, v8
	v_rcp_f32_e32 v182, v182
	v_mul_f32_e32 v162, v95, v162
	v_mul_f32_e32 v181, 0x3c000000, v162
	v_mul_f32_e32 v162, v96, v163
	v_add_f32_e32 v163, 1.0, v161
	v_rcp_f32_e32 v163, v163
	v_mul_f32_e32 v183, 0x3c000000, v162
	v_add_f32_e32 v5, 1.0, v158
	v_rcp_f32_e32 v5, v5
	v_mul_f32_e32 v162, v97, v163
	v_add_f32_e32 v163, 1.0, v9
	v_mul_f32_e32 v184, 0x3c000000, v162
	v_mul_f32_e32 v162, v90, v182
	v_rcp_f32_e32 v163, v163
	v_add_f32_e32 v182, 1.0, v156
	v_rcp_f32_e32 v182, v182
	v_mul_f32_e32 v185, 0x3c000000, v162
	v_mul_f32_e32 v162, v91, v163
	v_mul_f32_e32 v186, 0x3c000000, v162
	v_mul_f32_e32 v162, v92, v182
	v_mul_f32_e32 v182, 0x3c000000, v162
	v_add_f32_e32 v162, 1.0, v157
	v_mul_f32_e32 v5, v94, v5
	v_rcp_f32_e32 v187, v162
	v_mul_f32_e32 v5, 0x3c000000, v5
	v_mov_b32_e32 v162, 0
	v_mov_b32_e32 v163, 0
	v_cvt_pk_fp8_f32 v162, v5, v181
	v_cvt_pk_fp8_f32 v163, v185, v186
	v_mul_f32_e32 v5, v93, v187
	v_mul_f32_e32 v5, 0x3c000000, v5
	v_cvt_pk_fp8_f32 v162, v183, v184 op_sel:[0,0,1]
	v_cvt_pk_fp8_f32 v163, v182, v5 op_sel:[0,0,1]
	ds_write_b64 v180, v[162:163] offset:32
	s_cbranch_execz .LBB0_627

; #define LAS __attribute__((address_space(3)))
; __device__ __forceinline__ unsigned pk4_fp8(float a, float b, float c, float d) { int w = 0; w = __builtin_amdgcn_cvt_pk_fp8_f32(a, b, w, false); w = __builtin_amdgcn_cvt_pk_fp8_f32(c, d, w, true); return (unsigned)w; }
; __device__ __forceinline__ float bf_lo(unsigned w) { return __uint_as_float(w << 16); }
; __device__ __forceinline__ float bf_hi(unsigned w) { return __uint_as_float(w & 0xffff0000u); }
; __device__ __forceinline__ float sigmoidf_fast(float x) { return __builtin_amdgcn_rcpf(1.0f + __builtin_amdgcn_exp2f(-1.4426950408889634f * x)); }
;     __device__ __forceinline__ void operator()(f32x4 (&acc)[2][2][4][2], const Unit& u, int wr, int wc, int fr, int fq) const {
;     ...
;                 const size_t ro = (size_t)(u.row0 + ai * 128 + wr * 64 + m * 16 + fr) * DM + col0;
; #pragma unroll
;                 for (int bj = 0; bj < 2; ++bj) {
;                     const u32x4 gd = *(const u32x4*)(GDF + ro + bj * 32);
;                     const float ed[8] = {bf_lo(gd.x), bf_hi(gd.x), bf_lo(gd.y), bf_hi(gd.y), bf_lo(gd.z), bf_hi(gd.z), bf_lo(gd.w), bf_hi(gd.w)};
;                     if (u.tag == 0) {
;                         const u32x4 gn = *(const u32x4*)(GNA + ro + bj * 32);
;                         const float en[8] = {bf_lo(gn.x), bf_hi(gn.x), bf_lo(gn.y), bf_hi(gn.y), bf_lo(gn.z), bf_hi(gn.z), bf_lo(gn.w), bf_hi(gn.w)};
; #pragma unroll
;                         for (int e = 0; e < 8; ++e) {
;                             const float r = (1.0f + __builtin_amdgcn_exp2f(-1.4426950408889634f * ed[e])) * __builtin_amdgcn_rcpf(1.0f + __builtin_amdgcn_exp2f(-1.4426950408889634f * en[e]));
;                             acc[ai][bj][m][e >> 2][e & 3] *= r; }
;                     } else {
;                         float y[8];
; #pragma unroll
;                         for (int e = 0; e < 8; ++e) y[e] = acc[ai][bj][m][e >> 2][e & 3] * sigmoidf_fast(ed[e]) * (PSCALE * WSCALE_INV * OSCALE_INV);
;                         u32x2 w; w.x = pk4_fp8(y[0], y[1], y[2], y[3]); w.y = pk4_fp8(y[4], y[5], y[6], y[7]);
;                         *(LAS u32x2*)(my + fr * 80 + bj * 32 + fq * 8) = w;
.LBB0_577:
	s_nop 1
	v_add_u32_e32 v6, s76, v171
	v_ashrrev_i32_e32 v7, 31, v6
	v_lshlrev_b64 v[6:7], 11, v[6:7]
	v_lshl_add_u64 v[6:7], v[6:7], 0, v[2:3]
	v_lshl_add_u64 v[8:9], v[6:7], 1, s[40:41]
	v_add_u32_e32 v248, 0x80, v4
	v_ashrrev_i32_e32 v249, 31, v248
	v_lshlrev_b64 v[248:249], 11, v[248:249]
	v_lshl_add_u64 v[248:249], v[248:249], 0, v[2:3]
	v_lshl_add_u64 v[250:251], v[248:249], 1, s[40:41]
	global_load_dwordx4 v[210:213], v[250:251], off nt
	global_load_dwordx4 v[214:217], v[250:251], off offset:64 nt
	v_lshl_add_u64 v[250:251], v[248:249], 1, s[38:39]
	global_load_dwordx4 v[218:221], v[250:251], off nt
	global_load_dwordx4 v[222:225], v[250:251], off offset:64 nt
	s_and_b64 vcc, exec, s[4:5]
	s_mov_b64 s[58:59], -1
	s_waitcnt vmcnt(8)
	v_mov_b64_e32 v[156:157], v[226:227]
	v_mov_b64_e32 v[158:159], v[228:229]
	v_lshlrev_b32_e32 v5, 16, v156
	v_and_b32_e32 v156, 0xffff0000, v156
	v_lshlrev_b32_e32 v160, 16, v157
	v_and_b32_e32 v157, 0xffff0000, v157
	v_lshlrev_b32_e32 v161, 16, v158
	v_and_b32_e32 v158, 0xffff0000, v158
	v_lshlrev_b32_e32 v162, 16, v159
	v_and_b32_e32 v159, 0xffff0000, v159
	v_mul_f32_e32 v5, 0xbfb8aa3b, v5
	v_mul_f32_e32 v156, 0xbfb8aa3b, v156
	v_mul_f32_e32 v163, 0xbfb8aa3b, v160
	v_mul_f32_e32 v157, 0xbfb8aa3b, v157
	v_mul_f32_e32 v181, 0xbfb8aa3b, v161
	v_mul_f32_e32 v158, 0xbfb8aa3b, v158
	v_mul_f32_e32 v182, 0xbfb8aa3b, v162
	v_mul_f32_e32 v159, 0xbfb8aa3b, v159
	v_exp_f32_e32 v160, v5
	v_exp_f32_e32 v161, v156
	v_exp_f32_e32 v162, v163
	v_exp_f32_e32 v163, v157
	v_exp_f32_e32 v156, v181
	v_exp_f32_e32 v157, v158
	v_exp_f32_e32 v158, v182
	v_exp_f32_e32 v159, v159
	s_cbranch_vccnz .LBB0_579
	v_add_f32_e32 v182, 1.0, v162
	v_rcp_f32_e32 v182, v182
	v_add_f32_e32 v183, 1.0, v163
	v_rcp_f32_e32 v183, v183
	v_add_f32_e32 v184, 1.0, v156
	v_rcp_f32_e32 v184, v184
	v_mul_f32_e32 v182, v120, v182
	v_mul_f32_e32 v185, 0x3c000000, v182
	v_mul_f32_e32 v182, v121, v183
	v_add_f32_e32 v183, 1.0, v157
	v_mul_f32_e32 v186, 0x3c000000, v182
	v_mul_f32_e32 v182, v114, v184
	v_rcp_f32_e32 v183, v183
	v_add_f32_e32 v184, 1.0, v158
	v_rcp_f32_e32 v184, v184
	v_add_f32_e32 v5, 1.0, v160
	v_add_f32_e32 v181, 1.0, v161
	v_rcp_f32_e32 v5, v5
	v_rcp_f32_e32 v181, v181
	v_mul_f32_e32 v187, 0x3c000000, v182
	v_mul_f32_e32 v182, v115, v183
	v_mul_f32_e32 v188, 0x3c000000, v182
	v_mul_f32_e32 v182, v116, v184
	v_mul_f32_e32 v184, 0x3c000000, v182
	v_add_f32_e32 v182, 1.0, v159
	v_mul_f32_e32 v5, v118, v5
	v_mul_f32_e32 v181, v119, v181
	v_rcp_f32_e32 v189, v182
	v_mul_f32_e32 v5, 0x3c000000, v5
	v_mul_f32_e32 v181, 0x3c000000, v181
	v_mov_b32_e32 v182, 0
	v_mov_b32_e32 v183, 0
	v_cvt_pk_fp8_f32 v182, v5, v181
	v_cvt_pk_fp8_f32 v183, v187, v188
	v_mul_f32_e32 v5, v117, v189
	v_mul_f32_e32 v5, 0x3c000000, v5
	v_cvt_pk_fp8_f32 v182, v185, v186 op_sel:[0,0,1]
	v_cvt_pk_fp8_f32 v183, v184, v5 op_sel:[0,0,1]
	s_mov_b64 s[58:59], 0
	ds_write_b64 v180, v[182:183]
; #define LAS __attribute__((address_space(3)))
; __device__ __forceinline__ unsigned pk4_fp8(float a, float b, float c, float d) { int w = 0; w = __builtin_amdgcn_cvt_pk_fp8_f32(a, b, w, false); w = __builtin_amdgcn_cvt_pk_fp8_f32(c, d, w, true); return (unsigned)w; }
; __device__ __forceinline__ float bf_lo(unsigned w) { return __uint_as_float(w << 16); }
; __device__ __forceinline__ float bf_hi(unsigned w) { return __uint_as_float(w & 0xffff0000u); }
; __device__ __forceinline__ float sigmoidf_fast(float x) { return __builtin_amdgcn_rcpf(1.0f + __builtin_amdgcn_exp2f(-1.4426950408889634f * x)); }
;     __device__ __forceinline__ void operator()(f32x4 (&acc)[2][2][4][2], const Unit& u, int wr, int wc, int fr, int fq) const {
;     ...
;                 const size_t ro = (size_t)(u.row0 + ai * 128 + wr * 64 + m * 16 + fr) * DM + col0;
; #pragma unroll
;                 for (int bj = 0; bj < 2; ++bj) {
;                     const u32x4 gd = *(const u32x4*)(GDF + ro + bj * 32);
;                     const float ed[8] = {bf_lo(gd.x), bf_hi(gd.x), bf_lo(gd.y), bf_hi(gd.y), bf_lo(gd.z), bf_hi(gd.z), bf_lo(gd.w), bf_hi(gd.w)};
;                     if (u.tag == 0) {
;                         const u32x4 gn = *(const u32x4*)(GNA + ro + bj * 32);
;                         const float en[8] = {bf_lo(gn.x), bf_hi(gn.x), bf_lo(gn.y), bf_hi(gn.y), bf_lo(gn.z), bf_hi(gn.z), bf_lo(gn.w), bf_hi(gn.w)};
; #pragma unroll
;                         for (int e = 0; e < 8; ++e) {
;                             const float r = (1.0f + __builtin_amdgcn_exp2f(-1.4426950408889634f * ed[e])) * __builtin_amdgcn_rcpf(1.0f + __builtin_amdgcn_exp2f(-1.4426950408889634f * en[e]));
;                             acc[ai][bj][m][e >> 2][e & 3] *= r; }
;                     } else {
;                         float y[8];
; #pragma unroll
;                         for (int e = 0; e < 8; ++e) y[e] = acc[ai][bj][m][e >> 2][e & 3] * sigmoidf_fast(ed[e]) * (PSCALE * WSCALE_INV * OSCALE_INV);
;                         u32x2 w; w.x = pk4_fp8(y[0], y[1], y[2], y[3]); w.y = pk4_fp8(y[4], y[5], y[6], y[7]);
;                         *(LAS u32x2*)(my + fr * 80 + bj * 32 + fq * 8) = w;
.LBB0_579:
	s_andn2_b64 vcc, exec, s[58:59]
	v_lshl_add_u64 v[6:7], v[6:7], 1, s[38:39]
	s_cbranch_vccnz .LBB0_581
	v_pk_add_f32 v[162:163], v[162:163], 1.0 op_sel_hi:[1,0]
	v_pk_add_f32 v[160:161], v[160:161], 1.0 op_sel_hi:[1,0]
	v_pk_add_f32 v[158:159], v[158:159], 1.0 op_sel_hi:[1,0]
	v_pk_add_f32 v[156:157], v[156:157], 1.0 op_sel_hi:[1,0]
	s_waitcnt vmcnt(8)
	v_mov_b64_e32 v[182:183], v[234:235]
	v_mov_b64_e32 v[184:185], v[236:237]
	v_lshlrev_b32_e32 v5, 16, v182
	v_and_b32_e32 v181, 0xffff0000, v182
	v_lshlrev_b32_e32 v182, 16, v183
	v_and_b32_e32 v183, 0xffff0000, v183
	v_lshlrev_b32_e32 v186, 16, v184
	v_and_b32_e32 v184, 0xffff0000, v184
	v_lshlrev_b32_e32 v187, 16, v185
	v_and_b32_e32 v185, 0xffff0000, v185
	v_mul_f32_e32 v5, 0xbfb8aa3b, v5
	v_mul_f32_e32 v181, 0xbfb8aa3b, v181
	v_mul_f32_e32 v182, 0xbfb8aa3b, v182
	v_mul_f32_e32 v183, 0xbfb8aa3b, v183
	v_mul_f32_e32 v186, 0xbfb8aa3b, v186
	v_mul_f32_e32 v184, 0xbfb8aa3b, v184
	v_mul_f32_e32 v187, 0xbfb8aa3b, v187
	v_mul_f32_e32 v185, 0xbfb8aa3b, v185
	v_exp_f32_e32 v5, v5
	v_exp_f32_e32 v181, v181
	v_exp_f32_e32 v182, v182
	v_exp_f32_e32 v183, v183
	v_exp_f32_e32 v186, v186
	v_exp_f32_e32 v184, v184
	v_exp_f32_e32 v187, v187
	v_exp_f32_e32 v185, v185
	v_add_f32_e32 v5, 1.0, v5
	v_add_f32_e32 v181, 1.0, v181
	v_add_f32_e32 v188, 1.0, v182
	v_add_f32_e32 v189, 1.0, v183
	v_add_f32_e32 v186, 1.0, v186
	v_add_f32_e32 v190, 1.0, v184
	v_add_f32_e32 v191, 1.0, v187
	v_add_f32_e32 v192, 1.0, v185
	v_rcp_f32_e32 v182, v5
	v_rcp_f32_e32 v183, v181
	v_rcp_f32_e32 v184, v188
	v_rcp_f32_e32 v185, v189
	v_rcp_f32_e32 v186, v186
	v_rcp_f32_e32 v187, v190
	v_rcp_f32_e32 v188, v191
	v_rcp_f32_e32 v189, v192
	v_pk_mul_f32 v[160:161], v[160:161], v[182:183]
	v_pk_mul_f32 v[162:163], v[162:163], v[184:185]
	v_pk_mul_f32 v[156:157], v[156:157], v[186:187]
	v_pk_mul_f32 v[158:159], v[158:159], v[188:189]
	v_pk_mul_f32 v[120:121], v[120:121], v[162:163]
	v_pk_mul_f32 v[118:119], v[118:119], v[160:161]
	v_pk_mul_f32 v[116:117], v[116:117], v[158:159]
	v_pk_mul_f32 v[114:115], v[114:115], v[156:157]
.LBB0_581:
	s_and_b64 vcc, exec, s[4:5]
	s_mov_b64 s[58:59], -1
	s_waitcnt vmcnt(8)
	v_mov_b64_e32 v[156:157], v[230:231]
	v_mov_b64_e32 v[158:159], v[232:233]
	v_lshlrev_b32_e32 v5, 16, v156
	v_and_b32_e32 v8, 0xffff0000, v156
	v_lshlrev_b32_e32 v9, 16, v157
	v_and_b32_e32 v156, 0xffff0000, v157
	v_lshlrev_b32_e32 v157, 16, v158
	v_and_b32_e32 v158, 0xffff0000, v158
	v_lshlrev_b32_e32 v160, 16, v159
	v_and_b32_e32 v159, 0xffff0000, v159
	v_mul_f32_e32 v5, 0xbfb8aa3b, v5
	v_mul_f32_e32 v8, 0xbfb8aa3b, v8
	v_mul_f32_e32 v9, 0xbfb8aa3b, v9
	v_mul_f32_e32 v156, 0xbfb8aa3b, v156
	v_mul_f32_e32 v157, 0xbfb8aa3b, v157
	v_mul_f32_e32 v162, 0xbfb8aa3b, v158
	v_mul_f32_e32 v163, 0xbfb8aa3b, v160
	v_mul_f32_e32 v181, 0xbfb8aa3b, v159
	v_exp_f32_e32 v158, v5
	v_exp_f32_e32 v159, v8
	v_exp_f32_e32 v160, v9
	v_exp_f32_e32 v161, v156
	v_exp_f32_e32 v8, v157
	v_exp_f32_e32 v9, v162
	v_exp_f32_e32 v156, v163
	v_exp_f32_e32 v157, v181
	s_cbranch_vccnz .LBB0_628
	v_add_f32_e32 v162, 1.0, v159
	v_add_f32_e32 v163, 1.0, v160
	v_rcp_f32_e32 v162, v162
	v_rcp_f32_e32 v163, v163
	v_add_f32_e32 v182, 1.0, v8
	v_rcp_f32_e32 v182, v182
	v_mul_f32_e32 v162, v87, v162
	v_mul_f32_e32 v181, 0x3c000000, v162
	v_mul_f32_e32 v162, v88, v163
	v_add_f32_e32 v163, 1.0, v161
	v_rcp_f32_e32 v163, v163
	v_mul_f32_e32 v183, 0x3c000000, v162
	v_add_f32_e32 v5, 1.0, v158
	v_rcp_f32_e32 v5, v5
	v_mul_f32_e32 v162, v89, v163
	v_add_f32_e32 v163, 1.0, v9
	v_mul_f32_e32 v184, 0x3c000000, v162
	v_mul_f32_e32 v162, v82, v182
	v_rcp_f32_e32 v163, v163
	v_add_f32_e32 v182, 1.0, v156
	v_rcp_f32_e32 v182, v182
	v_mul_f32_e32 v185, 0x3c000000, v162
	v_mul_f32_e32 v162, v83, v163
	v_mul_f32_e32 v186, 0x3c000000, v162
	v_mul_f32_e32 v162, v84, v182
	v_mul_f32_e32 v182, 0x3c000000, v162
	v_add_f32_e32 v162, 1.0, v157
	v_mul_f32_e32 v5, v86, v5
	v_rcp_f32_e32 v187, v162
	v_mul_f32_e32 v5, 0x3c000000, v5
	v_mov_b32_e32 v162, 0
	v_mov_b32_e32 v163, 0
	v_cvt_pk_fp8_f32 v162, v5, v181
	v_cvt_pk_fp8_f32 v163, v185, v186
	v_mul_f32_e32 v5, v85, v187
	v_mul_f32_e32 v5, 0x3c000000, v5
	v_cvt_pk_fp8_f32 v162, v183, v184 op_sel:[0,0,1]
	v_cvt_pk_fp8_f32 v163, v182, v5 op_sel:[0,0,1]
	ds_write_b64 v180, v[162:163] offset:32
	s_cbranch_execz .LBB0_629

; #define LAS __attribute__((address_space(3)))
; __device__ __forceinline__ unsigned pk4_fp8(float a, float b, float c, float d) { int w = 0; w = __builtin_amdgcn_cvt_pk_fp8_f32(a, b, w, false); w = __builtin_amdgcn_cvt_pk_fp8_f32(c, d, w, true); return (unsigned)w; }
; __device__ __forceinline__ float bf_lo(unsigned w) { return __uint_as_float(w << 16); }
; __device__ __forceinline__ float bf_hi(unsigned w) { return __uint_as_float(w & 0xffff0000u); }
; __device__ __forceinline__ float sigmoidf_fast(float x) { return __builtin_amdgcn_rcpf(1.0f + __builtin_amdgcn_exp2f(-1.4426950408889634f * x)); }
;     __device__ __forceinline__ void operator()(f32x4 (&acc)[2][2][4][2], const Unit& u, int wr, int wc, int fr, int fq) const {
;     ...
;                 const size_t ro = (size_t)(u.row0 + ai * 128 + wr * 64 + m * 16 + fr) * DM + col0;
; #pragma unroll
;                 for (int bj = 0; bj < 2; ++bj) {
;                     const u32x4 gd = *(const u32x4*)(GDF + ro + bj * 32);
;                     const float ed[8] = {bf_lo(gd.x), bf_hi(gd.x), bf_lo(gd.y), bf_hi(gd.y), bf_lo(gd.z), bf_hi(gd.z), bf_lo(gd.w), bf_hi(gd.w)};
;                     if (u.tag == 0) {
;                         const u32x4 gn = *(const u32x4*)(GNA + ro + bj * 32);
;                         const float en[8] = {bf_lo(gn.x), bf_hi(gn.x), bf_lo(gn.y), bf_hi(gn.y), bf_lo(gn.z), bf_hi(gn.z), bf_lo(gn.w), bf_hi(gn.w)};
; #pragma unroll
;                         for (int e = 0; e < 8; ++e) {
;                             const float r = (1.0f + __builtin_amdgcn_exp2f(-1.4426950408889634f * ed[e])) * __builtin_amdgcn_rcpf(1.0f + __builtin_amdgcn_exp2f(-1.4426950408889634f * en[e]));
;                             acc[ai][bj][m][e >> 2][e & 3] *= r; }
;                     } else {
;                         float y[8];
; #pragma unroll
;                         for (int e = 0; e < 8; ++e) y[e] = acc[ai][bj][m][e >> 2][e & 3] * sigmoidf_fast(ed[e]) * (PSCALE * WSCALE_INV * OSCALE_INV);
;                         u32x2 w; w.x = pk4_fp8(y[0], y[1], y[2], y[3]); w.y = pk4_fp8(y[4], y[5], y[6], y[7]);
;                         *(LAS u32x2*)(my + fr * 80 + bj * 32 + fq * 8) = w;
.LBB0_585:
	s_nop 1
	v_add_u32_e32 v6, s76, v173
	v_ashrrev_i32_e32 v7, 31, v6
	v_lshlrev_b64 v[6:7], 11, v[6:7]
	v_lshl_add_u64 v[6:7], v[6:7], 0, v[2:3]
	v_lshl_add_u64 v[8:9], v[6:7], 1, s[40:41]
	v_add_u32_e32 v248, 0x90, v4
	v_ashrrev_i32_e32 v249, 31, v248
	v_lshlrev_b64 v[248:249], 11, v[248:249]
	v_lshl_add_u64 v[248:249], v[248:249], 0, v[2:3]
	v_lshl_add_u64 v[250:251], v[248:249], 1, s[40:41]
	global_load_dwordx4 v[226:229], v[250:251], off nt
	global_load_dwordx4 v[230:233], v[250:251], off offset:64 nt
	v_lshl_add_u64 v[250:251], v[248:249], 1, s[38:39]
	global_load_dwordx4 v[234:237], v[250:251], off nt
	global_load_dwordx4 v[238:241], v[250:251], off offset:64 nt
	s_and_b64 vcc, exec, s[4:5]
	s_mov_b64 s[58:59], -1
	s_waitcnt vmcnt(8)
	v_mov_b64_e32 v[156:157], v[194:195]
	v_mov_b64_e32 v[158:159], v[196:197]
	v_lshlrev_b32_e32 v5, 16, v156
	v_and_b32_e32 v156, 0xffff0000, v156
	v_lshlrev_b32_e32 v160, 16, v157
	v_and_b32_e32 v157, 0xffff0000, v157
	v_lshlrev_b32_e32 v161, 16, v158
	v_and_b32_e32 v158, 0xffff0000, v158
	v_lshlrev_b32_e32 v162, 16, v159
	v_and_b32_e32 v159, 0xffff0000, v159
	v_mul_f32_e32 v5, 0xbfb8aa3b, v5
	v_mul_f32_e32 v156, 0xbfb8aa3b, v156
	v_mul_f32_e32 v163, 0xbfb8aa3b, v160
	v_mul_f32_e32 v157, 0xbfb8aa3b, v157
	v_mul_f32_e32 v181, 0xbfb8aa3b, v161
	v_mul_f32_e32 v158, 0xbfb8aa3b, v158
	v_mul_f32_e32 v182, 0xbfb8aa3b, v162
	v_mul_f32_e32 v159, 0xbfb8aa3b, v159
	v_exp_f32_e32 v160, v5
	v_exp_f32_e32 v161, v156
	v_exp_f32_e32 v162, v163
	v_exp_f32_e32 v163, v157
	v_exp_f32_e32 v156, v181
	v_exp_f32_e32 v157, v158
	v_exp_f32_e32 v158, v182
	v_exp_f32_e32 v159, v159
	s_cbranch_vccnz .LBB0_587
	v_add_f32_e32 v182, 1.0, v162
	v_rcp_f32_e32 v182, v182
	v_add_f32_e32 v183, 1.0, v163
	v_rcp_f32_e32 v183, v183
	v_add_f32_e32 v184, 1.0, v156
	v_rcp_f32_e32 v184, v184
	v_mul_f32_e32 v182, v112, v182
	v_mul_f32_e32 v185, 0x3c000000, v182
	v_mul_f32_e32 v182, v113, v183
	v_add_f32_e32 v183, 1.0, v157
	v_mul_f32_e32 v186, 0x3c000000, v182
	v_mul_f32_e32 v182, v106, v184
	v_rcp_f32_e32 v183, v183
	v_add_f32_e32 v184, 1.0, v158
	v_rcp_f32_e32 v184, v184
	v_add_f32_e32 v5, 1.0, v160
	v_add_f32_e32 v181, 1.0, v161
	v_rcp_f32_e32 v5, v5
	v_rcp_f32_e32 v181, v181
	v_mul_f32_e32 v187, 0x3c000000, v182
	v_mul_f32_e32 v182, v107, v183
	v_mul_f32_e32 v188, 0x3c000000, v182
	v_mul_f32_e32 v182, v108, v184
	v_mul_f32_e32 v184, 0x3c000000, v182
	v_add_f32_e32 v182, 1.0, v159
	v_mul_f32_e32 v5, v110, v5
	v_mul_f32_e32 v181, v111, v181
	v_rcp_f32_e32 v189, v182
	v_mul_f32_e32 v5, 0x3c000000, v5
	v_mul_f32_e32 v181, 0x3c000000, v181
	v_mov_b32_e32 v182, 0
	v_mov_b32_e32 v183, 0
	v_cvt_pk_fp8_f32 v182, v5, v181
	v_cvt_pk_fp8_f32 v183, v187, v188
	v_mul_f32_e32 v5, v109, v189
	v_mul_f32_e32 v5, 0x3c000000, v5
	v_cvt_pk_fp8_f32 v182, v185, v186 op_sel:[0,0,1]
	v_cvt_pk_fp8_f32 v183, v184, v5 op_sel:[0,0,1]
	s_mov_b64 s[58:59], 0
	ds_write_b64 v180, v[182:183]
; #define LAS __attribute__((address_space(3)))
; __device__ __forceinline__ unsigned pk4_fp8(float a, float b, float c, float d) { int w = 0; w = __builtin_amdgcn_cvt_pk_fp8_f32(a, b, w, false); w = __builtin_amdgcn_cvt_pk_fp8_f32(c, d, w, true); return (unsigned)w; }
; __device__ __forceinline__ float bf_lo(unsigned w) { return __uint_as_float(w << 16); }
; __device__ __forceinline__ float bf_hi(unsigned w) { return __uint_as_float(w & 0xffff0000u); }
; __device__ __forceinline__ float sigmoidf_fast(float x) { return __builtin_amdgcn_rcpf(1.0f + __builtin_amdgcn_exp2f(-1.4426950408889634f * x)); }
;     __device__ __forceinline__ void operator()(f32x4 (&acc)[2][2][4][2], const Unit& u, int wr, int wc, int fr, int fq) const {
;     ...
;                 const size_t ro = (size_t)(u.row0 + ai * 128 + wr * 64 + m * 16 + fr) * DM + col0;
; #pragma unroll
;                 for (int bj = 0; bj < 2; ++bj) {
;                     const u32x4 gd = *(const u32x4*)(GDF + ro + bj * 32);
;                     const float ed[8] = {bf_lo(gd.x), bf_hi(gd.x), bf_lo(gd.y), bf_hi(gd.y), bf_lo(gd.z), bf_hi(gd.z), bf_lo(gd.w), bf_hi(gd.w)};
;                     if (u.tag == 0) {
;                         const u32x4 gn = *(const u32x4*)(GNA + ro + bj * 32);
;                         const float en[8] = {bf_lo(gn.x), bf_hi(gn.x), bf_lo(gn.y), bf_hi(gn.y), bf_lo(gn.z), bf_hi(gn.z), bf_lo(gn.w), bf_hi(gn.w)};
; #pragma unroll
;                         for (int e = 0; e < 8; ++e) {
;                             const float r = (1.0f + __builtin_amdgcn_exp2f(-1.4426950408889634f * ed[e])) * __builtin_amdgcn_rcpf(1.0f + __builtin_amdgcn_exp2f(-1.4426950408889634f * en[e]));
;                             acc[ai][bj][m][e >> 2][e & 3] *= r; }
;                     } else {
;                         float y[8];
; #pragma unroll
;                         for (int e = 0; e < 8; ++e) y[e] = acc[ai][bj][m][e >> 2][e & 3] * sigmoidf_fast(ed[e]) * (PSCALE * WSCALE_INV * OSCALE_INV);
;                         u32x2 w; w.x = pk4_fp8(y[0], y[1], y[2], y[3]); w.y = pk4_fp8(y[4], y[5], y[6], y[7]);
;                         *(LAS u32x2*)(my + fr * 80 + bj * 32 + fq * 8) = w;
.LBB0_587:
	s_andn2_b64 vcc, exec, s[58:59]
	v_lshl_add_u64 v[6:7], v[6:7], 1, s[38:39]
	s_cbranch_vccnz .LBB0_589
	v_pk_add_f32 v[162:163], v[162:163], 1.0 op_sel_hi:[1,0]
	v_pk_add_f32 v[160:161], v[160:161], 1.0 op_sel_hi:[1,0]
	v_pk_add_f32 v[158:159], v[158:159], 1.0 op_sel_hi:[1,0]
	v_pk_add_f32 v[156:157], v[156:157], 1.0 op_sel_hi:[1,0]
	s_waitcnt vmcnt(8)
	v_mov_b64_e32 v[182:183], v[202:203]
	v_mov_b64_e32 v[184:185], v[204:205]
	v_lshlrev_b32_e32 v5, 16, v182
	v_and_b32_e32 v181, 0xffff0000, v182
	v_lshlrev_b32_e32 v182, 16, v183
	v_and_b32_e32 v183, 0xffff0000, v183
	v_lshlrev_b32_e32 v186, 16, v184
	v_and_b32_e32 v184, 0xffff0000, v184
	v_lshlrev_b32_e32 v187, 16, v185
	v_and_b32_e32 v185, 0xffff0000, v185
	v_mul_f32_e32 v5, 0xbfb8aa3b, v5
	v_mul_f32_e32 v181, 0xbfb8aa3b, v181
	v_mul_f32_e32 v182, 0xbfb8aa3b, v182
	v_mul_f32_e32 v183, 0xbfb8aa3b, v183
	v_mul_f32_e32 v186, 0xbfb8aa3b, v186
	v_mul_f32_e32 v184, 0xbfb8aa3b, v184
	v_mul_f32_e32 v187, 0xbfb8aa3b, v187
	v_mul_f32_e32 v185, 0xbfb8aa3b, v185
	v_exp_f32_e32 v5, v5
	v_exp_f32_e32 v181, v181
	v_exp_f32_e32 v182, v182
	v_exp_f32_e32 v183, v183
	v_exp_f32_e32 v186, v186
	v_exp_f32_e32 v184, v184
	v_exp_f32_e32 v187, v187
	v_exp_f32_e32 v185, v185
	v_add_f32_e32 v5, 1.0, v5
	v_add_f32_e32 v181, 1.0, v181
	v_add_f32_e32 v188, 1.0, v182
	v_add_f32_e32 v189, 1.0, v183
	v_add_f32_e32 v186, 1.0, v186
	v_add_f32_e32 v190, 1.0, v184
	v_add_f32_e32 v191, 1.0, v187
	v_add_f32_e32 v192, 1.0, v185
	v_rcp_f32_e32 v182, v5
	v_rcp_f32_e32 v183, v181
	v_rcp_f32_e32 v184, v188
	v_rcp_f32_e32 v185, v189
	v_rcp_f32_e32 v186, v186
	v_rcp_f32_e32 v187, v190
	v_rcp_f32_e32 v188, v191
	v_rcp_f32_e32 v189, v192
	v_pk_mul_f32 v[160:161], v[160:161], v[182:183]
	v_pk_mul_f32 v[162:163], v[162:163], v[184:185]
	v_pk_mul_f32 v[156:157], v[156:157], v[186:187]
	v_pk_mul_f32 v[158:159], v[158:159], v[188:189]
	v_pk_mul_f32 v[112:113], v[112:113], v[162:163]
	v_pk_mul_f32 v[110:111], v[110:111], v[160:161]
	v_pk_mul_f32 v[108:109], v[108:109], v[158:159]
	v_pk_mul_f32 v[106:107], v[106:107], v[156:157]
.LBB0_589:
	s_and_b64 vcc, exec, s[4:5]
	s_mov_b64 s[58:59], -1
	s_waitcnt vmcnt(8)
	v_mov_b64_e32 v[156:157], v[198:199]
	v_mov_b64_e32 v[158:159], v[200:201]
	v_lshlrev_b32_e32 v5, 16, v156
	v_and_b32_e32 v8, 0xffff0000, v156
	v_lshlrev_b32_e32 v9, 16, v157
	v_and_b32_e32 v156, 0xffff0000, v157
	v_lshlrev_b32_e32 v157, 16, v158
	v_and_b32_e32 v158, 0xffff0000, v158
	v_lshlrev_b32_e32 v160, 16, v159
	v_and_b32_e32 v159, 0xffff0000, v159
	v_mul_f32_e32 v5, 0xbfb8aa3b, v5
	v_mul_f32_e32 v8, 0xbfb8aa3b, v8
	v_mul_f32_e32 v9, 0xbfb8aa3b, v9
	v_mul_f32_e32 v156, 0xbfb8aa3b, v156
	v_mul_f32_e32 v157, 0xbfb8aa3b, v157
	v_mul_f32_e32 v162, 0xbfb8aa3b, v158
	v_mul_f32_e32 v163, 0xbfb8aa3b, v160
	v_mul_f32_e32 v181, 0xbfb8aa3b, v159
	v_exp_f32_e32 v158, v5
	v_exp_f32_e32 v159, v8
	v_exp_f32_e32 v160, v9
	v_exp_f32_e32 v161, v156
	v_exp_f32_e32 v8, v157
	v_exp_f32_e32 v9, v162
	v_exp_f32_e32 v156, v163
	v_exp_f32_e32 v157, v181
	s_cbranch_vccnz .LBB0_630
	v_add_f32_e32 v162, 1.0, v159
	v_add_f32_e32 v163, 1.0, v160
	v_rcp_f32_e32 v162, v162
	v_rcp_f32_e32 v163, v163
	v_add_f32_e32 v182, 1.0, v8
	v_rcp_f32_e32 v182, v182
	v_mul_f32_e32 v162, v79, v162
	v_mul_f32_e32 v181, 0x3c000000, v162
	v_mul_f32_e32 v162, v80, v163
	v_add_f32_e32 v163, 1.0, v161
	v_rcp_f32_e32 v163, v163
	v_mul_f32_e32 v183, 0x3c000000, v162
	v_add_f32_e32 v5, 1.0, v158
	v_rcp_f32_e32 v5, v5
	v_mul_f32_e32 v162, v81, v163
	v_add_f32_e32 v163, 1.0, v9
	v_mul_f32_e32 v184, 0x3c000000, v162
	v_mul_f32_e32 v162, v74, v182
	v_rcp_f32_e32 v163, v163
	v_add_f32_e32 v182, 1.0, v156
	v_rcp_f32_e32 v182, v182
	v_mul_f32_e32 v185, 0x3c000000, v162
	v_mul_f32_e32 v162, v75, v163
	v_mul_f32_e32 v186, 0x3c000000, v162
	v_mul_f32_e32 v162, v76, v182
	v_mul_f32_e32 v182, 0x3c000000, v162
	v_add_f32_e32 v162, 1.0, v157
	v_mul_f32_e32 v5, v78, v5
	v_rcp_f32_e32 v187, v162
	v_mul_f32_e32 v5, 0x3c000000, v5
	v_mov_b32_e32 v162, 0
	v_mov_b32_e32 v163, 0
	v_cvt_pk_fp8_f32 v162, v5, v181
	v_cvt_pk_fp8_f32 v163, v185, v186
	v_mul_f32_e32 v5, v77, v187
	v_mul_f32_e32 v5, 0x3c000000, v5
	v_cvt_pk_fp8_f32 v162, v183, v184 op_sel:[0,0,1]
	v_cvt_pk_fp8_f32 v163, v182, v5 op_sel:[0,0,1]
	ds_write_b64 v180, v[162:163] offset:32
	s_cbranch_execz .LBB0_631

; #define LAS __attribute__((address_space(3)))
; __device__ __forceinline__ unsigned pk4_fp8(float a, float b, float c, float d) { int w = 0; w = __builtin_amdgcn_cvt_pk_fp8_f32(a, b, w, false); w = __builtin_amdgcn_cvt_pk_fp8_f32(c, d, w, true); return (unsigned)w; }
; __device__ __forceinline__ float bf_lo(unsigned w) { return __uint_as_float(w << 16); }
; __device__ __forceinline__ float bf_hi(unsigned w) { return __uint_as_float(w & 0xffff0000u); }
; __device__ __forceinline__ float sigmoidf_fast(float x) { return __builtin_amdgcn_rcpf(1.0f + __builtin_amdgcn_exp2f(-1.4426950408889634f * x)); }
;     __device__ __forceinline__ void operator()(f32x4 (&acc)[2][2][4][2], const Unit& u, int wr, int wc, int fr, int fq) const {
;     ...
;                 const size_t ro = (size_t)(u.row0 + ai * 128 + wr * 64 + m * 16 + fr) * DM + col0;
; #pragma unroll
;                 for (int bj = 0; bj < 2; ++bj) {
;                     const u32x4 gd = *(const u32x4*)(GDF + ro + bj * 32);
;                     const float ed[8] = {bf_lo(gd.x), bf_hi(gd.x), bf_lo(gd.y), bf_hi(gd.y), bf_lo(gd.z), bf_hi(gd.z), bf_lo(gd.w), bf_hi(gd.w)};
;                     if (u.tag == 0) {
;                         const u32x4 gn = *(const u32x4*)(GNA + ro + bj * 32);
;                         const float en[8] = {bf_lo(gn.x), bf_hi(gn.x), bf_lo(gn.y), bf_hi(gn.y), bf_lo(gn.z), bf_hi(gn.z), bf_lo(gn.w), bf_hi(gn.w)};
; #pragma unroll
;                         for (int e = 0; e < 8; ++e) {
;                             const float r = (1.0f + __builtin_amdgcn_exp2f(-1.4426950408889634f * ed[e])) * __builtin_amdgcn_rcpf(1.0f + __builtin_amdgcn_exp2f(-1.4426950408889634f * en[e]));
;                             acc[ai][bj][m][e >> 2][e & 3] *= r; }
;                     } else {
;                         float y[8];
; #pragma unroll
;                         for (int e = 0; e < 8; ++e) y[e] = acc[ai][bj][m][e >> 2][e & 3] * sigmoidf_fast(ed[e]) * (PSCALE * WSCALE_INV * OSCALE_INV);
;                         u32x2 w; w.x = pk4_fp8(y[0], y[1], y[2], y[3]); w.y = pk4_fp8(y[4], y[5], y[6], y[7]);
;                         *(LAS u32x2*)(my + fr * 80 + bj * 32 + fq * 8) = w;
.LBB0_593:
	s_nop 1
	v_add_u32_e32 v6, 0x80, v4
	v_ashrrev_i32_e32 v7, 31, v6
	v_lshlrev_b64 v[6:7], 11, v[6:7]
	v_lshl_add_u64 v[6:7], v[6:7], 0, v[2:3]
	v_lshl_add_u64 v[8:9], v[6:7], 1, s[40:41]
	v_add_u32_e32 v248, 0xa0, v4
	v_ashrrev_i32_e32 v249, 31, v248
	v_lshlrev_b64 v[248:249], 11, v[248:249]
	v_lshl_add_u64 v[248:249], v[248:249], 0, v[2:3]
	v_lshl_add_u64 v[250:251], v[248:249], 1, s[40:41]
	global_load_dwordx4 v[194:197], v[250:251], off nt
	global_load_dwordx4 v[198:201], v[250:251], off offset:64 nt
	v_lshl_add_u64 v[250:251], v[248:249], 1, s[38:39]
	global_load_dwordx4 v[202:205], v[250:251], off nt
	global_load_dwordx4 v[206:209], v[250:251], off offset:64 nt
	s_and_b64 vcc, exec, s[4:5]
	s_mov_b64 s[58:59], -1
	s_waitcnt vmcnt(8)
	v_mov_b64_e32 v[156:157], v[210:211]
	v_mov_b64_e32 v[158:159], v[212:213]
	v_lshlrev_b32_e32 v5, 16, v156
	v_and_b32_e32 v156, 0xffff0000, v156
	v_lshlrev_b32_e32 v160, 16, v157
	v_and_b32_e32 v157, 0xffff0000, v157
	v_lshlrev_b32_e32 v161, 16, v158
	v_and_b32_e32 v158, 0xffff0000, v158
	v_lshlrev_b32_e32 v162, 16, v159
	v_and_b32_e32 v159, 0xffff0000, v159
	v_mul_f32_e32 v5, 0xbfb8aa3b, v5
	v_mul_f32_e32 v156, 0xbfb8aa3b, v156
	v_mul_f32_e32 v163, 0xbfb8aa3b, v160
	v_mul_f32_e32 v157, 0xbfb8aa3b, v157
	v_mul_f32_e32 v181, 0xbfb8aa3b, v161
	v_mul_f32_e32 v158, 0xbfb8aa3b, v158
	v_mul_f32_e32 v182, 0xbfb8aa3b, v162
	v_mul_f32_e32 v159, 0xbfb8aa3b, v159
	v_exp_f32_e32 v160, v5
	v_exp_f32_e32 v161, v156
	v_exp_f32_e32 v162, v163
	v_exp_f32_e32 v163, v157
	v_exp_f32_e32 v156, v181
	v_exp_f32_e32 v157, v158
	v_exp_f32_e32 v158, v182
	v_exp_f32_e32 v159, v159
	s_cbranch_vccnz .LBB0_595
	v_add_f32_e32 v182, 1.0, v162
	v_rcp_f32_e32 v182, v182
	v_add_f32_e32 v183, 1.0, v163
	v_rcp_f32_e32 v183, v183
	v_add_f32_e32 v184, 1.0, v156
	v_rcp_f32_e32 v184, v184
	v_mul_f32_e32 v182, v72, v182
	v_mul_f32_e32 v185, 0x3c000000, v182
	v_mul_f32_e32 v182, v73, v183
	v_add_f32_e32 v183, 1.0, v157
	v_mul_f32_e32 v186, 0x3c000000, v182
	v_mul_f32_e32 v182, v66, v184
	v_rcp_f32_e32 v183, v183
	v_add_f32_e32 v184, 1.0, v158
	v_rcp_f32_e32 v184, v184
	v_add_f32_e32 v5, 1.0, v160
	v_add_f32_e32 v181, 1.0, v161
	v_rcp_f32_e32 v5, v5
	v_rcp_f32_e32 v181, v181
	v_mul_f32_e32 v187, 0x3c000000, v182
	v_mul_f32_e32 v182, v67, v183
	v_mul_f32_e32 v188, 0x3c000000, v182
	v_mul_f32_e32 v182, v68, v184
	v_mul_f32_e32 v184, 0x3c000000, v182
	v_add_f32_e32 v182, 1.0, v159
	v_mul_f32_e32 v5, v70, v5
	v_mul_f32_e32 v181, v71, v181
	v_rcp_f32_e32 v189, v182
	v_mul_f32_e32 v5, 0x3c000000, v5
	v_mul_f32_e32 v181, 0x3c000000, v181
	v_mov_b32_e32 v182, 0
	v_mov_b32_e32 v183, 0
	v_cvt_pk_fp8_f32 v182, v5, v181
	v_cvt_pk_fp8_f32 v183, v187, v188
	v_mul_f32_e32 v5, v69, v189
	v_mul_f32_e32 v5, 0x3c000000, v5
	v_cvt_pk_fp8_f32 v182, v185, v186 op_sel:[0,0,1]
	v_cvt_pk_fp8_f32 v183, v184, v5 op_sel:[0,0,1]
	s_mov_b64 s[58:59], 0
	ds_write_b64 v180, v[182:183]
; #define LAS __attribute__((address_space(3)))
; __device__ __forceinline__ unsigned pk4_fp8(float a, float b, float c, float d) { int w = 0; w = __builtin_amdgcn_cvt_pk_fp8_f32(a, b, w, false); w = __builtin_amdgcn_cvt_pk_fp8_f32(c, d, w, true); return (unsigned)w; }
; __device__ __forceinline__ float bf_lo(unsigned w) { return __uint_as_float(w << 16); }
; __device__ __forceinline__ float bf_hi(unsigned w) { return __uint_as_float(w & 0xffff0000u); }
; __device__ __forceinline__ float sigmoidf_fast(float x) { return __builtin_amdgcn_rcpf(1.0f + __builtin_amdgcn_exp2f(-1.4426950408889634f * x)); }
;     __device__ __forceinline__ void operator()(f32x4 (&acc)[2][2][4][2], const Unit& u, int wr, int wc, int fr, int fq) const {
;     ...
;                 const size_t ro = (size_t)(u.row0 + ai * 128 + wr * 64 + m * 16 + fr) * DM + col0;
; #pragma unroll
;                 for (int bj = 0; bj < 2; ++bj) {
;                     const u32x4 gd = *(const u32x4*)(GDF + ro + bj * 32);
;                     const float ed[8] = {bf_lo(gd.x), bf_hi(gd.x), bf_lo(gd.y), bf_hi(gd.y), bf_lo(gd.z), bf_hi(gd.z), bf_lo(gd.w), bf_hi(gd.w)};
;                     if (u.tag == 0) {
;                         const u32x4 gn = *(const u32x4*)(GNA + ro + bj * 32);
;                         const float en[8] = {bf_lo(gn.x), bf_hi(gn.x), bf_lo(gn.y), bf_hi(gn.y), bf_lo(gn.z), bf_hi(gn.z), bf_lo(gn.w), bf_hi(gn.w)};
; #pragma unroll
;                         for (int e = 0; e < 8; ++e) {
;                             const float r = (1.0f + __builtin_amdgcn_exp2f(-1.4426950408889634f * ed[e])) * __builtin_amdgcn_rcpf(1.0f + __builtin_amdgcn_exp2f(-1.4426950408889634f * en[e]));
;                             acc[ai][bj][m][e >> 2][e & 3] *= r; }
;                     } else {
;                         float y[8];
; #pragma unroll
;                         for (int e = 0; e < 8; ++e) y[e] = acc[ai][bj][m][e >> 2][e & 3] * sigmoidf_fast(ed[e]) * (PSCALE * WSCALE_INV * OSCALE_INV);
;                         u32x2 w; w.x = pk4_fp8(y[0], y[1], y[2], y[3]); w.y = pk4_fp8(y[4], y[5], y[6], y[7]);
;                         *(LAS u32x2*)(my + fr * 80 + bj * 32 + fq * 8) = w;
.LBB0_595:
	s_andn2_b64 vcc, exec, s[58:59]
	v_lshl_add_u64 v[6:7], v[6:7], 1, s[38:39]
	s_cbranch_vccnz .LBB0_597
	v_pk_add_f32 v[162:163], v[162:163], 1.0 op_sel_hi:[1,0]
	v_pk_add_f32 v[160:161], v[160:161], 1.0 op_sel_hi:[1,0]
	v_pk_add_f32 v[158:159], v[158:159], 1.0 op_sel_hi:[1,0]
	v_pk_add_f32 v[156:157], v[156:157], 1.0 op_sel_hi:[1,0]
	s_waitcnt vmcnt(8)
	v_mov_b64_e32 v[182:183], v[218:219]
	v_mov_b64_e32 v[184:185], v[220:221]
	v_lshlrev_b32_e32 v5, 16, v182
	v_and_b32_e32 v181, 0xffff0000, v182
	v_lshlrev_b32_e32 v182, 16, v183
	v_and_b32_e32 v183, 0xffff0000, v183
	v_lshlrev_b32_e32 v186, 16, v184
	v_and_b32_e32 v184, 0xffff0000, v184
	v_lshlrev_b32_e32 v187, 16, v185
	v_and_b32_e32 v185, 0xffff0000, v185
	v_mul_f32_e32 v5, 0xbfb8aa3b, v5
	v_mul_f32_e32 v181, 0xbfb8aa3b, v181
	v_mul_f32_e32 v182, 0xbfb8aa3b, v182
	v_mul_f32_e32 v183, 0xbfb8aa3b, v183
	v_mul_f32_e32 v186, 0xbfb8aa3b, v186
	v_mul_f32_e32 v184, 0xbfb8aa3b, v184
	v_mul_f32_e32 v187, 0xbfb8aa3b, v187
	v_mul_f32_e32 v185, 0xbfb8aa3b, v185
	v_exp_f32_e32 v5, v5
	v_exp_f32_e32 v181, v181
	v_exp_f32_e32 v182, v182
	v_exp_f32_e32 v183, v183
	v_exp_f32_e32 v186, v186
	v_exp_f32_e32 v184, v184
	v_exp_f32_e32 v187, v187
	v_exp_f32_e32 v185, v185
	v_add_f32_e32 v5, 1.0, v5
	v_add_f32_e32 v181, 1.0, v181
	v_add_f32_e32 v188, 1.0, v182
	v_add_f32_e32 v189, 1.0, v183
	v_add_f32_e32 v186, 1.0, v186
	v_add_f32_e32 v190, 1.0, v184
	v_add_f32_e32 v191, 1.0, v187
	v_add_f32_e32 v192, 1.0, v185
	v_rcp_f32_e32 v182, v5
	v_rcp_f32_e32 v183, v181
	v_rcp_f32_e32 v184, v188
	v_rcp_f32_e32 v185, v189
	v_rcp_f32_e32 v186, v186
	v_rcp_f32_e32 v187, v190
	v_rcp_f32_e32 v188, v191
	v_rcp_f32_e32 v189, v192
	v_pk_mul_f32 v[160:161], v[160:161], v[182:183]
	v_pk_mul_f32 v[162:163], v[162:163], v[184:185]
	v_pk_mul_f32 v[156:157], v[156:157], v[186:187]
	v_pk_mul_f32 v[158:159], v[158:159], v[188:189]
	v_pk_mul_f32 v[72:73], v[72:73], v[162:163]
	v_pk_mul_f32 v[70:71], v[70:71], v[160:161]
	v_pk_mul_f32 v[68:69], v[68:69], v[158:159]
	v_pk_mul_f32 v[66:67], v[66:67], v[156:157]
.LBB0_597:
	s_and_b64 vcc, exec, s[4:5]
	s_mov_b64 s[58:59], -1
	s_waitcnt vmcnt(8)
	v_mov_b64_e32 v[156:157], v[214:215]
	v_mov_b64_e32 v[158:159], v[216:217]
	v_lshlrev_b32_e32 v5, 16, v156
	v_and_b32_e32 v8, 0xffff0000, v156
	v_lshlrev_b32_e32 v9, 16, v157
	v_and_b32_e32 v156, 0xffff0000, v157
	v_lshlrev_b32_e32 v157, 16, v158
	v_and_b32_e32 v158, 0xffff0000, v158
	v_lshlrev_b32_e32 v160, 16, v159
	v_and_b32_e32 v159, 0xffff0000, v159
	v_mul_f32_e32 v5, 0xbfb8aa3b, v5
	v_mul_f32_e32 v8, 0xbfb8aa3b, v8
	v_mul_f32_e32 v9, 0xbfb8aa3b, v9
	v_mul_f32_e32 v156, 0xbfb8aa3b, v156
	v_mul_f32_e32 v157, 0xbfb8aa3b, v157
	v_mul_f32_e32 v162, 0xbfb8aa3b, v158
	v_mul_f32_e32 v163, 0xbfb8aa3b, v160
	v_mul_f32_e32 v181, 0xbfb8aa3b, v159
	v_exp_f32_e32 v158, v5
	v_exp_f32_e32 v159, v8
	v_exp_f32_e32 v160, v9
	v_exp_f32_e32 v161, v156
	v_exp_f32_e32 v8, v157
	v_exp_f32_e32 v9, v162
	v_exp_f32_e32 v156, v163
	v_exp_f32_e32 v157, v181
	s_cbranch_vccnz .LBB0_632
	v_add_f32_e32 v162, 1.0, v159
	v_add_f32_e32 v163, 1.0, v160
	v_rcp_f32_e32 v162, v162
	v_rcp_f32_e32 v163, v163
	v_add_f32_e32 v182, 1.0, v8
	v_rcp_f32_e32 v182, v182
	v_mul_f32_e32 v162, v39, v162
	v_mul_f32_e32 v181, 0x3c000000, v162
	v_mul_f32_e32 v162, v40, v163
	v_add_f32_e32 v163, 1.0, v161
	v_rcp_f32_e32 v163, v163
	v_mul_f32_e32 v183, 0x3c000000, v162
	v_add_f32_e32 v5, 1.0, v158
	v_rcp_f32_e32 v5, v5
	v_mul_f32_e32 v162, v41, v163
	v_add_f32_e32 v163, 1.0, v9
	v_mul_f32_e32 v184, 0x3c000000, v162
	v_mul_f32_e32 v162, v34, v182
	v_rcp_f32_e32 v163, v163
	v_add_f32_e32 v182, 1.0, v156
	v_rcp_f32_e32 v182, v182
	v_mul_f32_e32 v185, 0x3c000000, v162
	v_mul_f32_e32 v162, v35, v163
	v_mul_f32_e32 v186, 0x3c000000, v162
	v_mul_f32_e32 v162, v36, v182
	v_mul_f32_e32 v182, 0x3c000000, v162
	v_add_f32_e32 v162, 1.0, v157
	v_mul_f32_e32 v5, v38, v5
	v_rcp_f32_e32 v187, v162
	v_mul_f32_e32 v5, 0x3c000000, v5
	v_mov_b32_e32 v162, 0
	v_mov_b32_e32 v163, 0
	v_cvt_pk_fp8_f32 v162, v5, v181
	v_cvt_pk_fp8_f32 v163, v185, v186
	v_mul_f32_e32 v5, v37, v187
	v_mul_f32_e32 v5, 0x3c000000, v5
	v_cvt_pk_fp8_f32 v162, v183, v184 op_sel:[0,0,1]
	v_cvt_pk_fp8_f32 v163, v182, v5 op_sel:[0,0,1]
	ds_write_b64 v180, v[162:163] offset:32
	s_cbranch_execz .LBB0_633

; #define LAS __attribute__((address_space(3)))
; __device__ __forceinline__ unsigned pk4_fp8(float a, float b, float c, float d) { int w = 0; w = __builtin_amdgcn_cvt_pk_fp8_f32(a, b, w, false); w = __builtin_amdgcn_cvt_pk_fp8_f32(c, d, w, true); return (unsigned)w; }
; __device__ __forceinline__ float bf_lo(unsigned w) { return __uint_as_float(w << 16); }
; __device__ __forceinline__ float bf_hi(unsigned w) { return __uint_as_float(w & 0xffff0000u); }
; __device__ __forceinline__ float sigmoidf_fast(float x) { return __builtin_amdgcn_rcpf(1.0f + __builtin_amdgcn_exp2f(-1.4426950408889634f * x)); }
;     __device__ __forceinline__ void operator()(f32x4 (&acc)[2][2][4][2], const Unit& u, int wr, int wc, int fr, int fq) const {
;     ...
;                 const size_t ro = (size_t)(u.row0 + ai * 128 + wr * 64 + m * 16 + fr) * DM + col0;
; #pragma unroll
;                 for (int bj = 0; bj < 2; ++bj) {
;                     const u32x4 gd = *(const u32x4*)(GDF + ro + bj * 32);
;                     const float ed[8] = {bf_lo(gd.x), bf_hi(gd.x), bf_lo(gd.y), bf_hi(gd.y), bf_lo(gd.z), bf_hi(gd.z), bf_lo(gd.w), bf_hi(gd.w)};
;                     if (u.tag == 0) {
;                         const u32x4 gn = *(const u32x4*)(GNA + ro + bj * 32);
;                         const float en[8] = {bf_lo(gn.x), bf_hi(gn.x), bf_lo(gn.y), bf_hi(gn.y), bf_lo(gn.z), bf_hi(gn.z), bf_lo(gn.w), bf_hi(gn.w)};
; #pragma unroll
;                         for (int e = 0; e < 8; ++e) {
;                             const float r = (1.0f + __builtin_amdgcn_exp2f(-1.4426950408889634f * ed[e])) * __builtin_amdgcn_rcpf(1.0f + __builtin_amdgcn_exp2f(-1.4426950408889634f * en[e]));
;                             acc[ai][bj][m][e >> 2][e & 3] *= r; }
;                     } else {
;                         float y[8];
; #pragma unroll
;                         for (int e = 0; e < 8; ++e) y[e] = acc[ai][bj][m][e >> 2][e & 3] * sigmoidf_fast(ed[e]) * (PSCALE * WSCALE_INV * OSCALE_INV);
;                         u32x2 w; w.x = pk4_fp8(y[0], y[1], y[2], y[3]); w.y = pk4_fp8(y[4], y[5], y[6], y[7]);
;                         *(LAS u32x2*)(my + fr * 80 + bj * 32 + fq * 8) = w;
.LBB0_601:
	s_nop 1
	v_add_u32_e32 v6, 0x90, v4
	v_ashrrev_i32_e32 v7, 31, v6
	v_lshlrev_b64 v[6:7], 11, v[6:7]
	v_lshl_add_u64 v[6:7], v[6:7], 0, v[2:3]
	v_lshl_add_u64 v[8:9], v[6:7], 1, s[40:41]
	v_add_u32_e32 v248, 0xb0, v4
	v_ashrrev_i32_e32 v249, 31, v248
	v_lshlrev_b64 v[248:249], 11, v[248:249]
	v_lshl_add_u64 v[248:249], v[248:249], 0, v[2:3]
	v_lshl_add_u64 v[250:251], v[248:249], 1, s[40:41]
	global_load_dwordx4 v[210:213], v[250:251], off nt
	global_load_dwordx4 v[214:217], v[250:251], off offset:64 nt
	v_lshl_add_u64 v[250:251], v[248:249], 1, s[38:39]
	global_load_dwordx4 v[218:221], v[250:251], off nt
	global_load_dwordx4 v[222:225], v[250:251], off offset:64 nt
	s_and_b64 vcc, exec, s[4:5]
	s_mov_b64 s[58:59], -1
	s_waitcnt vmcnt(8)
	v_mov_b64_e32 v[156:157], v[226:227]
	v_mov_b64_e32 v[158:159], v[228:229]
	v_lshlrev_b32_e32 v5, 16, v156
	v_and_b32_e32 v156, 0xffff0000, v156
	v_lshlrev_b32_e32 v160, 16, v157
	v_and_b32_e32 v157, 0xffff0000, v157
	v_lshlrev_b32_e32 v161, 16, v158
	v_and_b32_e32 v158, 0xffff0000, v158
	v_lshlrev_b32_e32 v162, 16, v159
	v_and_b32_e32 v159, 0xffff0000, v159
	v_mul_f32_e32 v5, 0xbfb8aa3b, v5
	v_mul_f32_e32 v156, 0xbfb8aa3b, v156
	v_mul_f32_e32 v163, 0xbfb8aa3b, v160
	v_mul_f32_e32 v157, 0xbfb8aa3b, v157
	v_mul_f32_e32 v181, 0xbfb8aa3b, v161
	v_mul_f32_e32 v158, 0xbfb8aa3b, v158
	v_mul_f32_e32 v182, 0xbfb8aa3b, v162
	v_mul_f32_e32 v159, 0xbfb8aa3b, v159
	v_exp_f32_e32 v160, v5
	v_exp_f32_e32 v161, v156
	v_exp_f32_e32 v162, v163
	v_exp_f32_e32 v163, v157
	v_exp_f32_e32 v156, v181
	v_exp_f32_e32 v157, v158
	v_exp_f32_e32 v158, v182
	v_exp_f32_e32 v159, v159
	s_cbranch_vccnz .LBB0_603
	v_add_f32_e32 v182, 1.0, v162
	v_rcp_f32_e32 v182, v182
	v_add_f32_e32 v183, 1.0, v163
	v_rcp_f32_e32 v183, v183
	v_add_f32_e32 v184, 1.0, v156
	v_rcp_f32_e32 v184, v184
	v_mul_f32_e32 v182, v64, v182
	v_mul_f32_e32 v185, 0x3c000000, v182
	v_mul_f32_e32 v182, v65, v183
	v_add_f32_e32 v183, 1.0, v157
	v_mul_f32_e32 v186, 0x3c000000, v182
	v_mul_f32_e32 v182, v58, v184
	v_rcp_f32_e32 v183, v183
	v_add_f32_e32 v184, 1.0, v158
	v_rcp_f32_e32 v184, v184
	v_add_f32_e32 v5, 1.0, v160
	v_add_f32_e32 v181, 1.0, v161
	v_rcp_f32_e32 v5, v5
	v_rcp_f32_e32 v181, v181
	v_mul_f32_e32 v187, 0x3c000000, v182
	v_mul_f32_e32 v182, v59, v183
	v_mul_f32_e32 v188, 0x3c000000, v182
	v_mul_f32_e32 v182, v60, v184
	v_mul_f32_e32 v184, 0x3c000000, v182
	v_add_f32_e32 v182, 1.0, v159
	v_mul_f32_e32 v5, v62, v5
	v_mul_f32_e32 v181, v63, v181
	v_rcp_f32_e32 v189, v182
	v_mul_f32_e32 v5, 0x3c000000, v5
	v_mul_f32_e32 v181, 0x3c000000, v181
	v_mov_b32_e32 v182, 0
	v_mov_b32_e32 v183, 0
	v_cvt_pk_fp8_f32 v182, v5, v181
	v_cvt_pk_fp8_f32 v183, v187, v188
	v_mul_f32_e32 v5, v61, v189
	v_mul_f32_e32 v5, 0x3c000000, v5
	v_cvt_pk_fp8_f32 v182, v185, v186 op_sel:[0,0,1]
	v_cvt_pk_fp8_f32 v183, v184, v5 op_sel:[0,0,1]
	s_mov_b64 s[58:59], 0
	ds_write_b64 v180, v[182:183]
; #define LAS __attribute__((address_space(3)))
; __device__ __forceinline__ unsigned pk4_fp8(float a, float b, float c, float d) { int w = 0; w = __builtin_amdgcn_cvt_pk_fp8_f32(a, b, w, false); w = __builtin_amdgcn_cvt_pk_fp8_f32(c, d, w, true); return (unsigned)w; }
; __device__ __forceinline__ float bf_lo(unsigned w) { return __uint_as_float(w << 16); }
; __device__ __forceinline__ float bf_hi(unsigned w) { return __uint_as_float(w & 0xffff0000u); }
; __device__ __forceinline__ float sigmoidf_fast(float x) { return __builtin_amdgcn_rcpf(1.0f + __builtin_amdgcn_exp2f(-1.4426950408889634f * x)); }
;     __device__ __forceinline__ void operator()(f32x4 (&acc)[2][2][4][2], const Unit& u, int wr, int wc, int fr, int fq) const {
;     ...
;                 const size_t ro = (size_t)(u.row0 + ai * 128 + wr * 64 + m * 16 + fr) * DM + col0;
; #pragma unroll
;                 for (int bj = 0; bj < 2; ++bj) {
;                     const u32x4 gd = *(const u32x4*)(GDF + ro + bj * 32);
;                     const float ed[8] = {bf_lo(gd.x), bf_hi(gd.x), bf_lo(gd.y), bf_hi(gd.y), bf_lo(gd.z), bf_hi(gd.z), bf_lo(gd.w), bf_hi(gd.w)};
;                     if (u.tag == 0) {
;                         const u32x4 gn = *(const u32x4*)(GNA + ro + bj * 32);
;                         const float en[8] = {bf_lo(gn.x), bf_hi(gn.x), bf_lo(gn.y), bf_hi(gn.y), bf_lo(gn.z), bf_hi(gn.z), bf_lo(gn.w), bf_hi(gn.w)};
; #pragma unroll
;                         for (int e = 0; e < 8; ++e) {
;                             const float r = (1.0f + __builtin_amdgcn_exp2f(-1.4426950408889634f * ed[e])) * __builtin_amdgcn_rcpf(1.0f + __builtin_amdgcn_exp2f(-1.4426950408889634f * en[e]));
;                             acc[ai][bj][m][e >> 2][e & 3] *= r; }
;                     } else {
;                         float y[8];
; #pragma unroll
;                         for (int e = 0; e < 8; ++e) y[e] = acc[ai][bj][m][e >> 2][e & 3] * sigmoidf_fast(ed[e]) * (PSCALE * WSCALE_INV * OSCALE_INV);
;                         u32x2 w; w.x = pk4_fp8(y[0], y[1], y[2], y[3]); w.y = pk4_fp8(y[4], y[5], y[6], y[7]);
;                         *(LAS u32x2*)(my + fr * 80 + bj * 32 + fq * 8) = w;
.LBB0_603:
	s_andn2_b64 vcc, exec, s[58:59]
	v_lshl_add_u64 v[6:7], v[6:7], 1, s[38:39]
	s_cbranch_vccnz .LBB0_605
	v_pk_add_f32 v[162:163], v[162:163], 1.0 op_sel_hi:[1,0]
	v_pk_add_f32 v[160:161], v[160:161], 1.0 op_sel_hi:[1,0]
	v_pk_add_f32 v[158:159], v[158:159], 1.0 op_sel_hi:[1,0]
	v_pk_add_f32 v[156:157], v[156:157], 1.0 op_sel_hi:[1,0]
	s_waitcnt vmcnt(8)
	v_mov_b64_e32 v[182:183], v[234:235]
	v_mov_b64_e32 v[184:185], v[236:237]
	v_lshlrev_b32_e32 v5, 16, v182
	v_and_b32_e32 v181, 0xffff0000, v182
	v_lshlrev_b32_e32 v182, 16, v183
	v_and_b32_e32 v183, 0xffff0000, v183
	v_lshlrev_b32_e32 v186, 16, v184
	v_and_b32_e32 v184, 0xffff0000, v184
	v_lshlrev_b32_e32 v187, 16, v185
	v_and_b32_e32 v185, 0xffff0000, v185
	v_mul_f32_e32 v5, 0xbfb8aa3b, v5
	v_mul_f32_e32 v181, 0xbfb8aa3b, v181
	v_mul_f32_e32 v182, 0xbfb8aa3b, v182
	v_mul_f32_e32 v183, 0xbfb8aa3b, v183
	v_mul_f32_e32 v186, 0xbfb8aa3b, v186
	v_mul_f32_e32 v184, 0xbfb8aa3b, v184
	v_mul_f32_e32 v187, 0xbfb8aa3b, v187
	v_mul_f32_e32 v185, 0xbfb8aa3b, v185
	v_exp_f32_e32 v5, v5
	v_exp_f32_e32 v181, v181
	v_exp_f32_e32 v182, v182
	v_exp_f32_e32 v183, v183
	v_exp_f32_e32 v186, v186
	v_exp_f32_e32 v184, v184
	v_exp_f32_e32 v187, v187
	v_exp_f32_e32 v185, v185
	v_add_f32_e32 v5, 1.0, v5
	v_add_f32_e32 v181, 1.0, v181
	v_add_f32_e32 v188, 1.0, v182
	v_add_f32_e32 v189, 1.0, v183
	v_add_f32_e32 v186, 1.0, v186
	v_add_f32_e32 v190, 1.0, v184
	v_add_f32_e32 v191, 1.0, v187
	v_add_f32_e32 v192, 1.0, v185
	v_rcp_f32_e32 v182, v5
	v_rcp_f32_e32 v183, v181
	v_rcp_f32_e32 v184, v188
	v_rcp_f32_e32 v185, v189
	v_rcp_f32_e32 v186, v186
	v_rcp_f32_e32 v187, v190
	v_rcp_f32_e32 v188, v191
	v_rcp_f32_e32 v189, v192
	v_pk_mul_f32 v[160:161], v[160:161], v[182:183]
	v_pk_mul_f32 v[162:163], v[162:163], v[184:185]
	v_pk_mul_f32 v[156:157], v[156:157], v[186:187]
	v_pk_mul_f32 v[158:159], v[158:159], v[188:189]
	v_pk_mul_f32 v[64:65], v[64:65], v[162:163]
	v_pk_mul_f32 v[62:63], v[62:63], v[160:161]
	v_pk_mul_f32 v[60:61], v[60:61], v[158:159]
	v_pk_mul_f32 v[58:59], v[58:59], v[156:157]
.LBB0_605:
	s_and_b64 vcc, exec, s[4:5]
	s_mov_b64 s[58:59], -1
	s_waitcnt vmcnt(8)
	v_mov_b64_e32 v[156:157], v[230:231]
	v_mov_b64_e32 v[158:159], v[232:233]
	v_lshlrev_b32_e32 v5, 16, v156
	v_and_b32_e32 v8, 0xffff0000, v156
	v_lshlrev_b32_e32 v9, 16, v157
	v_and_b32_e32 v156, 0xffff0000, v157
	v_lshlrev_b32_e32 v157, 16, v158
	v_and_b32_e32 v158, 0xffff0000, v158
	v_lshlrev_b32_e32 v160, 16, v159
	v_and_b32_e32 v159, 0xffff0000, v159
	v_mul_f32_e32 v5, 0xbfb8aa3b, v5
	v_mul_f32_e32 v8, 0xbfb8aa3b, v8
	v_mul_f32_e32 v9, 0xbfb8aa3b, v9
	v_mul_f32_e32 v156, 0xbfb8aa3b, v156
	v_mul_f32_e32 v157, 0xbfb8aa3b, v157
	v_mul_f32_e32 v162, 0xbfb8aa3b, v158
	v_mul_f32_e32 v163, 0xbfb8aa3b, v160
	v_mul_f32_e32 v181, 0xbfb8aa3b, v159
	v_exp_f32_e32 v158, v5
	v_exp_f32_e32 v159, v8
	v_exp_f32_e32 v160, v9
	v_exp_f32_e32 v161, v156
	v_exp_f32_e32 v8, v157
	v_exp_f32_e32 v9, v162
	v_exp_f32_e32 v156, v163
	v_exp_f32_e32 v157, v181
	s_cbranch_vccnz .LBB0_634
	v_add_f32_e32 v162, 1.0, v159
	v_add_f32_e32 v163, 1.0, v160
	v_rcp_f32_e32 v162, v162
	v_rcp_f32_e32 v163, v163
	v_add_f32_e32 v182, 1.0, v8
	v_rcp_f32_e32 v182, v182
	v_mul_f32_e32 v162, v31, v162
	v_mul_f32_e32 v181, 0x3c000000, v162
	v_mul_f32_e32 v162, v32, v163
	v_add_f32_e32 v163, 1.0, v161
	v_rcp_f32_e32 v163, v163
	v_mul_f32_e32 v183, 0x3c000000, v162
	v_add_f32_e32 v5, 1.0, v158
	v_rcp_f32_e32 v5, v5
	v_mul_f32_e32 v162, v33, v163
	v_add_f32_e32 v163, 1.0, v9
	v_mul_f32_e32 v184, 0x3c000000, v162
	v_mul_f32_e32 v162, v26, v182
	v_rcp_f32_e32 v163, v163
	v_add_f32_e32 v182, 1.0, v156
	v_rcp_f32_e32 v182, v182
	v_mul_f32_e32 v185, 0x3c000000, v162
	v_mul_f32_e32 v162, v27, v163
	v_mul_f32_e32 v186, 0x3c000000, v162
	v_mul_f32_e32 v162, v28, v182
	v_mul_f32_e32 v182, 0x3c000000, v162
	v_add_f32_e32 v162, 1.0, v157
	v_mul_f32_e32 v5, v30, v5
	v_rcp_f32_e32 v187, v162
	v_mul_f32_e32 v5, 0x3c000000, v5
	v_mov_b32_e32 v162, 0
	v_mov_b32_e32 v163, 0
	v_cvt_pk_fp8_f32 v162, v5, v181
	v_cvt_pk_fp8_f32 v163, v185, v186
	v_mul_f32_e32 v5, v29, v187
	v_mul_f32_e32 v5, 0x3c000000, v5
	v_cvt_pk_fp8_f32 v162, v183, v184 op_sel:[0,0,1]
	v_cvt_pk_fp8_f32 v163, v182, v5 op_sel:[0,0,1]
	ds_write_b64 v180, v[162:163] offset:32
	s_cbranch_execz .LBB0_635

; #define LAS __attribute__((address_space(3)))
; __device__ __forceinline__ unsigned pk4_fp8(float a, float b, float c, float d) { int w = 0; w = __builtin_amdgcn_cvt_pk_fp8_f32(a, b, w, false); w = __builtin_amdgcn_cvt_pk_fp8_f32(c, d, w, true); return (unsigned)w; }
; __device__ __forceinline__ float bf_lo(unsigned w) { return __uint_as_float(w << 16); }
; __device__ __forceinline__ float bf_hi(unsigned w) { return __uint_as_float(w & 0xffff0000u); }
; __device__ __forceinline__ float sigmoidf_fast(float x) { return __builtin_amdgcn_rcpf(1.0f + __builtin_amdgcn_exp2f(-1.4426950408889634f * x)); }
;     __device__ __forceinline__ void operator()(f32x4 (&acc)[2][2][4][2], const Unit& u, int wr, int wc, int fr, int fq) const {
;     ...
;                 const size_t ro = (size_t)(u.row0 + ai * 128 + wr * 64 + m * 16 + fr) * DM + col0;
; #pragma unroll
;                 for (int bj = 0; bj < 2; ++bj) {
;                     const u32x4 gd = *(const u32x4*)(GDF + ro + bj * 32);
;                     const float ed[8] = {bf_lo(gd.x), bf_hi(gd.x), bf_lo(gd.y), bf_hi(gd.y), bf_lo(gd.z), bf_hi(gd.z), bf_lo(gd.w), bf_hi(gd.w)};
;                     if (u.tag == 0) {
;                         const u32x4 gn = *(const u32x4*)(GNA + ro + bj * 32);
;                         const float en[8] = {bf_lo(gn.x), bf_hi(gn.x), bf_lo(gn.y), bf_hi(gn.y), bf_lo(gn.z), bf_hi(gn.z), bf_lo(gn.w), bf_hi(gn.w)};
; #pragma unroll
;                         for (int e = 0; e < 8; ++e) {
;                             const float r = (1.0f + __builtin_amdgcn_exp2f(-1.4426950408889634f * ed[e])) * __builtin_amdgcn_rcpf(1.0f + __builtin_amdgcn_exp2f(-1.4426950408889634f * en[e]));
;                             acc[ai][bj][m][e >> 2][e & 3] *= r; }
;                     } else {
;                         float y[8];
; #pragma unroll
;                         for (int e = 0; e < 8; ++e) y[e] = acc[ai][bj][m][e >> 2][e & 3] * sigmoidf_fast(ed[e]) * (PSCALE * WSCALE_INV * OSCALE_INV);
;                         u32x2 w; w.x = pk4_fp8(y[0], y[1], y[2], y[3]); w.y = pk4_fp8(y[4], y[5], y[6], y[7]);
;                         *(LAS u32x2*)(my + fr * 80 + bj * 32 + fq * 8) = w;
.LBB0_609:
	s_nop 1
	v_add_u32_e32 v6, 0xa0, v4
	v_ashrrev_i32_e32 v7, 31, v6
	v_lshlrev_b64 v[6:7], 11, v[6:7]
	v_lshl_add_u64 v[6:7], v[6:7], 0, v[2:3]
	v_lshl_add_u64 v[8:9], v[6:7], 1, s[40:41]
	s_and_b64 vcc, exec, s[4:5]
	s_mov_b64 s[58:59], -1
	s_waitcnt vmcnt(4)
	v_mov_b64_e32 v[156:157], v[194:195]
	v_mov_b64_e32 v[158:159], v[196:197]
	v_lshlrev_b32_e32 v5, 16, v156
	v_and_b32_e32 v156, 0xffff0000, v156
	v_lshlrev_b32_e32 v160, 16, v157
	v_and_b32_e32 v157, 0xffff0000, v157
	v_lshlrev_b32_e32 v161, 16, v158
	v_and_b32_e32 v158, 0xffff0000, v158
	v_lshlrev_b32_e32 v162, 16, v159
	v_and_b32_e32 v159, 0xffff0000, v159
	v_mul_f32_e32 v5, 0xbfb8aa3b, v5
	v_mul_f32_e32 v156, 0xbfb8aa3b, v156
	v_mul_f32_e32 v163, 0xbfb8aa3b, v160
	v_mul_f32_e32 v157, 0xbfb8aa3b, v157
	v_mul_f32_e32 v181, 0xbfb8aa3b, v161
	v_mul_f32_e32 v158, 0xbfb8aa3b, v158
	v_mul_f32_e32 v182, 0xbfb8aa3b, v162
	v_mul_f32_e32 v159, 0xbfb8aa3b, v159
	v_exp_f32_e32 v160, v5
	v_exp_f32_e32 v161, v156
	v_exp_f32_e32 v162, v163
	v_exp_f32_e32 v163, v157
	v_exp_f32_e32 v156, v181
	v_exp_f32_e32 v157, v158
	v_exp_f32_e32 v158, v182
	v_exp_f32_e32 v159, v159
	s_cbranch_vccnz .LBB0_611
	v_add_f32_e32 v182, 1.0, v162
	v_rcp_f32_e32 v182, v182
	v_add_f32_e32 v183, 1.0, v163
	v_rcp_f32_e32 v183, v183
	v_add_f32_e32 v184, 1.0, v156
	v_rcp_f32_e32 v184, v184
	v_mul_f32_e32 v182, v56, v182
	v_mul_f32_e32 v185, 0x3c000000, v182
	v_mul_f32_e32 v182, v57, v183
	v_add_f32_e32 v183, 1.0, v157
	v_mul_f32_e32 v186, 0x3c000000, v182
	v_mul_f32_e32 v182, v50, v184
	v_rcp_f32_e32 v183, v183
	v_add_f32_e32 v184, 1.0, v158
	v_rcp_f32_e32 v184, v184
	v_add_f32_e32 v5, 1.0, v160
	v_add_f32_e32 v181, 1.0, v161
	v_rcp_f32_e32 v5, v5
	v_rcp_f32_e32 v181, v181
	v_mul_f32_e32 v187, 0x3c000000, v182
	v_mul_f32_e32 v182, v51, v183
	v_mul_f32_e32 v188, 0x3c000000, v182
	v_mul_f32_e32 v182, v52, v184
	v_mul_f32_e32 v184, 0x3c000000, v182
	v_add_f32_e32 v182, 1.0, v159
	v_mul_f32_e32 v5, v54, v5
	v_mul_f32_e32 v181, v55, v181
	v_rcp_f32_e32 v189, v182
	v_mul_f32_e32 v5, 0x3c000000, v5
	v_mul_f32_e32 v181, 0x3c000000, v181
	v_mov_b32_e32 v182, 0
	v_mov_b32_e32 v183, 0
	v_cvt_pk_fp8_f32 v182, v5, v181
	v_cvt_pk_fp8_f32 v183, v187, v188
	v_mul_f32_e32 v5, v53, v189
	v_mul_f32_e32 v5, 0x3c000000, v5
	v_cvt_pk_fp8_f32 v182, v185, v186 op_sel:[0,0,1]
	v_cvt_pk_fp8_f32 v183, v184, v5 op_sel:[0,0,1]
	s_mov_b64 s[58:59], 0
	ds_write_b64 v180, v[182:183]
.LBB0_611:
	s_andn2_b64 vcc, exec, s[58:59]
	v_lshl_add_u64 v[6:7], v[6:7], 1, s[38:39]
	s_cbranch_vccnz .LBB0_613
	v_pk_add_f32 v[162:163], v[162:163], 1.0 op_sel_hi:[1,0]
	v_pk_add_f32 v[160:161], v[160:161], 1.0 op_sel_hi:[1,0]
	v_pk_add_f32 v[158:159], v[158:159], 1.0 op_sel_hi:[1,0]
	v_pk_add_f32 v[156:157], v[156:157], 1.0 op_sel_hi:[1,0]
	s_waitcnt vmcnt(4)
	v_mov_b64_e32 v[182:183], v[202:203]
	v_mov_b64_e32 v[184:185], v[204:205]
	v_lshlrev_b32_e32 v5, 16, v182
	v_and_b32_e32 v181, 0xffff0000, v182
	v_lshlrev_b32_e32 v182, 16, v183
	v_and_b32_e32 v183, 0xffff0000, v183
	v_lshlrev_b32_e32 v186, 16, v184
	v_and_b32_e32 v184, 0xffff0000, v184
	v_lshlrev_b32_e32 v187, 16, v185
	v_and_b32_e32 v185, 0xffff0000, v185
	v_mul_f32_e32 v5, 0xbfb8aa3b, v5
	v_mul_f32_e32 v181, 0xbfb8aa3b, v181
	v_mul_f32_e32 v182, 0xbfb8aa3b, v182
	v_mul_f32_e32 v183, 0xbfb8aa3b, v183
	v_mul_f32_e32 v186, 0xbfb8aa3b, v186
	v_mul_f32_e32 v184, 0xbfb8aa3b, v184
	v_mul_f32_e32 v187, 0xbfb8aa3b, v187
	v_mul_f32_e32 v185, 0xbfb8aa3b, v185
	v_exp_f32_e32 v5, v5
	v_exp_f32_e32 v181, v181
	v_exp_f32_e32 v182, v182
	v_exp_f32_e32 v183, v183
	v_exp_f32_e32 v186, v186
	v_exp_f32_e32 v184, v184
	v_exp_f32_e32 v187, v187
	v_exp_f32_e32 v185, v185
	v_add_f32_e32 v5, 1.0, v5
	v_add_f32_e32 v181, 1.0, v181
	v_add_f32_e32 v188, 1.0, v182
	v_add_f32_e32 v189, 1.0, v183
	v_add_f32_e32 v186, 1.0, v186
	v_add_f32_e32 v190, 1.0, v184
	v_add_f32_e32 v191, 1.0, v187
	v_add_f32_e32 v192, 1.0, v185
	v_rcp_f32_e32 v182, v5
	v_rcp_f32_e32 v183, v181
	v_rcp_f32_e32 v184, v188
	v_rcp_f32_e32 v185, v189
	v_rcp_f32_e32 v186, v186
	v_rcp_f32_e32 v187, v190
	v_rcp_f32_e32 v188, v191
	v_rcp_f32_e32 v189, v192
	v_pk_mul_f32 v[160:161], v[160:161], v[182:183]
	v_pk_mul_f32 v[162:163], v[162:163], v[184:185]
	v_pk_mul_f32 v[156:157], v[156:157], v[186:187]
	v_pk_mul_f32 v[158:159], v[158:159], v[188:189]
	v_pk_mul_f32 v[56:57], v[56:57], v[162:163]
	v_pk_mul_f32 v[54:55], v[54:55], v[160:161]
	v_pk_mul_f32 v[52:53], v[52:53], v[158:159]
	v_pk_mul_f32 v[50:51], v[50:51], v[156:157]
.LBB0_613:
	s_and_b64 vcc, exec, s[4:5]
	s_mov_b64 s[58:59], -1
	s_waitcnt vmcnt(4)
	v_mov_b64_e32 v[156:157], v[198:199]
	v_mov_b64_e32 v[158:159], v[200:201]
	v_lshlrev_b32_e32 v5, 16, v156
	v_and_b32_e32 v8, 0xffff0000, v156
	v_lshlrev_b32_e32 v9, 16, v157
	v_and_b32_e32 v156, 0xffff0000, v157
	v_lshlrev_b32_e32 v157, 16, v158
	v_and_b32_e32 v158, 0xffff0000, v158
	v_lshlrev_b32_e32 v160, 16, v159
	v_and_b32_e32 v159, 0xffff0000, v159
	v_mul_f32_e32 v5, 0xbfb8aa3b, v5
	v_mul_f32_e32 v8, 0xbfb8aa3b, v8
	v_mul_f32_e32 v9, 0xbfb8aa3b, v9
	v_mul_f32_e32 v156, 0xbfb8aa3b, v156
	v_mul_f32_e32 v157, 0xbfb8aa3b, v157
	v_mul_f32_e32 v162, 0xbfb8aa3b, v158
	v_mul_f32_e32 v163, 0xbfb8aa3b, v160
	v_mul_f32_e32 v181, 0xbfb8aa3b, v159
	v_exp_f32_e32 v158, v5
	v_exp_f32_e32 v159, v8
	v_exp_f32_e32 v160, v9
	v_exp_f32_e32 v161, v156
	v_exp_f32_e32 v8, v157
	v_exp_f32_e32 v9, v162
	v_exp_f32_e32 v156, v163
	v_exp_f32_e32 v157, v181
	s_cbranch_vccnz .LBB0_636
	v_add_f32_e32 v162, 1.0, v159
	v_add_f32_e32 v163, 1.0, v160
	v_rcp_f32_e32 v162, v162
	v_rcp_f32_e32 v163, v163
	v_add_f32_e32 v182, 1.0, v8
	v_rcp_f32_e32 v182, v182
	v_mul_f32_e32 v162, v23, v162
	v_mul_f32_e32 v181, 0x3c000000, v162
	v_mul_f32_e32 v162, v24, v163
	v_add_f32_e32 v163, 1.0, v161
	v_rcp_f32_e32 v163, v163
	v_mul_f32_e32 v183, 0x3c000000, v162
	v_add_f32_e32 v5, 1.0, v158
	v_rcp_f32_e32 v5, v5
	v_mul_f32_e32 v162, v25, v163
	v_add_f32_e32 v163, 1.0, v9
	v_mul_f32_e32 v184, 0x3c000000, v162
	v_mul_f32_e32 v162, v18, v182
	v_rcp_f32_e32 v163, v163
	v_add_f32_e32 v182, 1.0, v156
	v_rcp_f32_e32 v182, v182
	v_mul_f32_e32 v185, 0x3c000000, v162
	v_mul_f32_e32 v162, v19, v163
	v_mul_f32_e32 v186, 0x3c000000, v162
	v_mul_f32_e32 v162, v20, v182
	v_mul_f32_e32 v182, 0x3c000000, v162
	v_add_f32_e32 v162, 1.0, v157
	v_mul_f32_e32 v5, v22, v5
	v_rcp_f32_e32 v187, v162
	v_mul_f32_e32 v5, 0x3c000000, v5
	v_mov_b32_e32 v162, 0
	v_mov_b32_e32 v163, 0
	v_cvt_pk_fp8_f32 v162, v5, v181
	v_cvt_pk_fp8_f32 v163, v185, v186
	v_mul_f32_e32 v5, v21, v187
	v_mul_f32_e32 v5, 0x3c000000, v5
	v_cvt_pk_fp8_f32 v162, v183, v184 op_sel:[0,0,1]
	v_cvt_pk_fp8_f32 v163, v182, v5 op_sel:[0,0,1]
	ds_write_b64 v180, v[162:163] offset:32
	s_cbranch_execz .LBB0_637

; #define LAS __attribute__((address_space(3)))
; __device__ __forceinline__ unsigned pk4_fp8(float a, float b, float c, float d) { int w = 0; w = __builtin_amdgcn_cvt_pk_fp8_f32(a, b, w, false); w = __builtin_amdgcn_cvt_pk_fp8_f32(c, d, w, true); return (unsigned)w; }
; __device__ __forceinline__ float bf_lo(unsigned w) { return __uint_as_float(w << 16); }
; __device__ __forceinline__ float bf_hi(unsigned w) { return __uint_as_float(w & 0xffff0000u); }
; __device__ __forceinline__ float sigmoidf_fast(float x) { return __builtin_amdgcn_rcpf(1.0f + __builtin_amdgcn_exp2f(-1.4426950408889634f * x)); }
;     __device__ __forceinline__ void operator()(f32x4 (&acc)[2][2][4][2], const Unit& u, int wr, int wc, int fr, int fq) const {
;     ...
;                 const size_t ro = (size_t)(u.row0 + ai * 128 + wr * 64 + m * 16 + fr) * DM + col0;
; #pragma unroll
;                 for (int bj = 0; bj < 2; ++bj) {
;                     const u32x4 gd = *(const u32x4*)(GDF + ro + bj * 32);
;                     const float ed[8] = {bf_lo(gd.x), bf_hi(gd.x), bf_lo(gd.y), bf_hi(gd.y), bf_lo(gd.z), bf_hi(gd.z), bf_lo(gd.w), bf_hi(gd.w)};
;                     if (u.tag == 0) {
;                         const u32x4 gn = *(const u32x4*)(GNA + ro + bj * 32);
;                         const float en[8] = {bf_lo(gn.x), bf_hi(gn.x), bf_lo(gn.y), bf_hi(gn.y), bf_lo(gn.z), bf_hi(gn.z), bf_lo(gn.w), bf_hi(gn.w)};
; #pragma unroll
;                         for (int e = 0; e < 8; ++e) {
;                             const float r = (1.0f + __builtin_amdgcn_exp2f(-1.4426950408889634f * ed[e])) * __builtin_amdgcn_rcpf(1.0f + __builtin_amdgcn_exp2f(-1.4426950408889634f * en[e]));
;                             acc[ai][bj][m][e >> 2][e & 3] *= r; }
;                     } else {
;                         float y[8];
; #pragma unroll
;                         for (int e = 0; e < 8; ++e) y[e] = acc[ai][bj][m][e >> 2][e & 3] * sigmoidf_fast(ed[e]) * (PSCALE * WSCALE_INV * OSCALE_INV);
;                         u32x2 w; w.x = pk4_fp8(y[0], y[1], y[2], y[3]); w.y = pk4_fp8(y[4], y[5], y[6], y[7]);
;                         *(LAS u32x2*)(my + fr * 80 + bj * 32 + fq * 8) = w;
.LBB0_617:
	v_add_u32_e32 v4, 0xb0, v4
	v_ashrrev_i32_e32 v5, 31, v4
	v_lshlrev_b64 v[4:5], 11, v[4:5]
	v_lshl_add_u64 v[2:3], v[4:5], 0, v[2:3]
	v_lshl_add_u64 v[4:5], v[2:3], 1, s[40:41]
	s_and_b64 vcc, exec, s[4:5]
	s_mov_b64 s[58:59], -1
	s_waitcnt vmcnt(0)
	v_mov_b64_e32 v[6:7], v[210:211]
	v_mov_b64_e32 v[8:9], v[212:213]
	v_lshlrev_b32_e32 v156, 16, v6
	v_and_b32_e32 v6, 0xffff0000, v6
	v_lshlrev_b32_e32 v157, 16, v7
	v_and_b32_e32 v7, 0xffff0000, v7
	v_lshlrev_b32_e32 v158, 16, v8
	v_and_b32_e32 v8, 0xffff0000, v8
	v_lshlrev_b32_e32 v159, 16, v9
	v_and_b32_e32 v9, 0xffff0000, v9
	v_mul_f32_e32 v156, 0xbfb8aa3b, v156
	v_mul_f32_e32 v6, 0xbfb8aa3b, v6
	v_mul_f32_e32 v160, 0xbfb8aa3b, v157
	v_mul_f32_e32 v7, 0xbfb8aa3b, v7
	v_mul_f32_e32 v161, 0xbfb8aa3b, v158
	v_mul_f32_e32 v8, 0xbfb8aa3b, v8
	v_mul_f32_e32 v162, 0xbfb8aa3b, v159
	v_mul_f32_e32 v9, 0xbfb8aa3b, v9
	v_exp_f32_e32 v156, v156
	v_exp_f32_e32 v157, v6
	v_exp_f32_e32 v158, v160
	v_exp_f32_e32 v159, v7
	v_exp_f32_e32 v6, v161
	v_exp_f32_e32 v7, v8
	v_exp_f32_e32 v8, v162
	v_exp_f32_e32 v9, v9
	s_cbranch_vccnz .LBB0_619
	v_add_f32_e32 v160, 1.0, v156
	v_rcp_f32_e32 v160, v160
	v_add_f32_e32 v161, 1.0, v157
	v_add_f32_e32 v162, 1.0, v158
	v_rcp_f32_e32 v161, v161
	v_rcp_f32_e32 v162, v162
	v_mul_f32_e32 v160, v46, v160
	v_mul_f32_e32 v163, 0x3c000000, v160
	v_mul_f32_e32 v160, v47, v161
	v_mul_f32_e32 v161, 0x3c000000, v160
	v_mul_f32_e32 v160, v48, v162
	v_add_f32_e32 v162, 1.0, v159
	v_rcp_f32_e32 v162, v162
	v_add_f32_e32 v181, 1.0, v6
	v_rcp_f32_e32 v181, v181
	v_mul_f32_e32 v182, 0x3c000000, v160
	v_mul_f32_e32 v160, v49, v162
	v_mul_f32_e32 v162, 0x3c000000, v160
	v_mul_f32_e32 v160, v42, v181
	v_add_f32_e32 v181, 1.0, v7
	v_rcp_f32_e32 v181, v181
	v_add_f32_e32 v183, 1.0, v8
	v_rcp_f32_e32 v183, v183
	v_mul_f32_e32 v184, 0x3c000000, v160
	v_mul_f32_e32 v160, v43, v181
	v_mul_f32_e32 v181, 0x3c000000, v160
	v_mul_f32_e32 v160, v44, v183
	v_mul_f32_e32 v183, 0x3c000000, v160
	v_add_f32_e32 v160, 1.0, v9
	v_rcp_f32_e32 v185, v160
	v_mov_b32_e32 v160, 0
	v_cvt_pk_fp8_f32 v160, v163, v161
	v_mov_b32_e32 v161, 0
	v_cvt_pk_fp8_f32 v161, v184, v181
	v_mul_f32_e32 v163, v45, v185
	v_mul_f32_e32 v163, 0x3c000000, v163
	v_cvt_pk_fp8_f32 v160, v182, v162 op_sel:[0,0,1]
	v_cvt_pk_fp8_f32 v161, v183, v163 op_sel:[0,0,1]
	s_mov_b64 s[58:59], 0
	ds_write_b64 v180, v[160:161]
.LBB0_619:
	s_andn2_b64 vcc, exec, s[58:59]
	v_lshl_add_u64 v[2:3], v[2:3], 1, s[38:39]
	s_cbranch_vccnz .LBB0_621
	v_pk_add_f32 v[158:159], v[158:159], 1.0 op_sel_hi:[1,0]
	v_pk_add_f32 v[156:157], v[156:157], 1.0 op_sel_hi:[1,0]
	v_pk_add_f32 v[8:9], v[8:9], 1.0 op_sel_hi:[1,0]
	v_pk_add_f32 v[6:7], v[6:7], 1.0 op_sel_hi:[1,0]
	s_waitcnt vmcnt(0)
	v_mov_b64_e32 v[160:161], v[218:219]
	v_mov_b64_e32 v[162:163], v[220:221]
	v_lshlrev_b32_e32 v181, 16, v160
	v_and_b32_e32 v160, 0xffff0000, v160
	v_lshlrev_b32_e32 v182, 16, v161
	v_and_b32_e32 v161, 0xffff0000, v161
	v_lshlrev_b32_e32 v183, 16, v162
	v_and_b32_e32 v162, 0xffff0000, v162
	v_lshlrev_b32_e32 v184, 16, v163
	v_and_b32_e32 v163, 0xffff0000, v163
	v_mul_f32_e32 v181, 0xbfb8aa3b, v181
	v_mul_f32_e32 v160, 0xbfb8aa3b, v160
	v_mul_f32_e32 v182, 0xbfb8aa3b, v182
	v_mul_f32_e32 v161, 0xbfb8aa3b, v161
	v_mul_f32_e32 v183, 0xbfb8aa3b, v183
	v_mul_f32_e32 v162, 0xbfb8aa3b, v162
	v_mul_f32_e32 v184, 0xbfb8aa3b, v184
	v_mul_f32_e32 v163, 0xbfb8aa3b, v163
	v_exp_f32_e32 v181, v181
	v_exp_f32_e32 v160, v160
	v_exp_f32_e32 v182, v182
	v_exp_f32_e32 v161, v161
	v_exp_f32_e32 v183, v183
	v_exp_f32_e32 v162, v162
	v_exp_f32_e32 v184, v184
	v_exp_f32_e32 v163, v163
	v_add_f32_e32 v181, 1.0, v181
	v_add_f32_e32 v185, 1.0, v160
	v_add_f32_e32 v182, 1.0, v182
	v_add_f32_e32 v186, 1.0, v161
	v_add_f32_e32 v183, 1.0, v183
	v_add_f32_e32 v187, 1.0, v162
	v_add_f32_e32 v184, 1.0, v184
	v_add_f32_e32 v188, 1.0, v163
	v_rcp_f32_e32 v160, v181
	v_rcp_f32_e32 v161, v185
	v_rcp_f32_e32 v162, v182
	v_rcp_f32_e32 v163, v186
	v_rcp_f32_e32 v182, v183
	v_rcp_f32_e32 v183, v187
	v_rcp_f32_e32 v184, v184
	v_rcp_f32_e32 v185, v188
	v_pk_mul_f32 v[156:157], v[156:157], v[160:161]
	v_pk_mul_f32 v[158:159], v[158:159], v[162:163]
	v_pk_mul_f32 v[6:7], v[6:7], v[182:183]
	v_pk_mul_f32 v[8:9], v[8:9], v[184:185]
	v_pk_mul_f32 v[48:49], v[48:49], v[158:159]
	v_pk_mul_f32 v[46:47], v[46:47], v[156:157]
	v_pk_mul_f32 v[44:45], v[44:45], v[8:9]
	v_pk_mul_f32 v[42:43], v[42:43], v[6:7]
.LBB0_621:
	s_and_b64 vcc, exec, s[4:5]
	s_mov_b64 s[4:5], -1
	s_waitcnt vmcnt(0)
	v_mov_b64_e32 v[4:5], v[214:215]
	v_mov_b64_e32 v[6:7], v[216:217]
	v_lshlrev_b32_e32 v8, 16, v4
	v_and_b32_e32 v4, 0xffff0000, v4
	v_lshlrev_b32_e32 v9, 16, v5
	v_and_b32_e32 v5, 0xffff0000, v5
	v_lshlrev_b32_e32 v156, 16, v6
	v_and_b32_e32 v6, 0xffff0000, v6
	v_lshlrev_b32_e32 v157, 16, v7
	v_and_b32_e32 v7, 0xffff0000, v7
	v_mul_f32_e32 v8, 0xbfb8aa3b, v8
	v_mul_f32_e32 v4, 0xbfb8aa3b, v4
	v_mul_f32_e32 v158, 0xbfb8aa3b, v9
	v_mul_f32_e32 v5, 0xbfb8aa3b, v5
	v_mul_f32_e32 v159, 0xbfb8aa3b, v156
	v_mul_f32_e32 v6, 0xbfb8aa3b, v6
	v_mul_f32_e32 v160, 0xbfb8aa3b, v157
	v_mul_f32_e32 v7, 0xbfb8aa3b, v7
	v_exp_f32_e32 v8, v8
	v_exp_f32_e32 v9, v4
	v_exp_f32_e32 v156, v158
	v_exp_f32_e32 v157, v5
	v_exp_f32_e32 v4, v159
	v_exp_f32_e32 v5, v6
	v_exp_f32_e32 v6, v160
	v_exp_f32_e32 v7, v7
	s_cbranch_vccnz .LBB0_638
	v_add_f32_e32 v158, 1.0, v8
	v_rcp_f32_e32 v158, v158
	v_add_f32_e32 v159, 1.0, v9
	v_add_f32_e32 v160, 1.0, v156
	v_rcp_f32_e32 v159, v159
	v_rcp_f32_e32 v160, v160
	v_mul_f32_e32 v158, v14, v158
	v_mul_f32_e32 v161, 0x3c000000, v158
	v_mul_f32_e32 v158, v15, v159
	v_mul_f32_e32 v159, 0x3c000000, v158
	v_mul_f32_e32 v158, v16, v160
	v_add_f32_e32 v160, 1.0, v157
	v_rcp_f32_e32 v160, v160
	v_add_f32_e32 v162, 1.0, v4
	v_rcp_f32_e32 v162, v162
	v_mul_f32_e32 v163, 0x3c000000, v158
	v_mul_f32_e32 v158, v17, v160
	v_mul_f32_e32 v160, 0x3c000000, v158
	v_mul_f32_e32 v158, v10, v162
	v_add_f32_e32 v162, 1.0, v5
	v_rcp_f32_e32 v162, v162
	v_add_f32_e32 v181, 1.0, v6
	v_rcp_f32_e32 v181, v181
	v_mul_f32_e32 v182, 0x3c000000, v158
	v_mul_f32_e32 v158, v11, v162
	v_mul_f32_e32 v162, 0x3c000000, v158
	v_mul_f32_e32 v158, v12, v181
	v_mul_f32_e32 v181, 0x3c000000, v158
	v_add_f32_e32 v158, 1.0, v7
	v_rcp_f32_e32 v183, v158
	v_mov_b32_e32 v158, 0
	v_cvt_pk_fp8_f32 v158, v161, v159
	v_mov_b32_e32 v159, 0
	v_cvt_pk_fp8_f32 v159, v182, v162
	v_mul_f32_e32 v161, v13, v183
	v_mul_f32_e32 v161, 0x3c000000, v161
	v_cvt_pk_fp8_f32 v158, v163, v160 op_sel:[0,0,1]
	v_cvt_pk_fp8_f32 v159, v181, v161 op_sel:[0,0,1]
	ds_write_b64 v180, v[158:159] offset:32
	s_cbranch_execz .LBB0_639

; __device__ __forceinline__ float bf_lo(unsigned w) { return __uint_as_float(w << 16); }
; __device__ __forceinline__ float bf_hi(unsigned w) { return __uint_as_float(w & 0xffff0000u); }
;     __device__ __forceinline__ void operator()(f32x4 (&acc)[2][2][4][2], const Unit& u, int wr, int wc, int fr, int fq) const {
;     ...
;                     if (u.tag == 0) {
;                         const u32x4 gn = *(const u32x4*)(GNA + ro + bj * 32);
;                         const float en[8] = {bf_lo(gn.x), bf_hi(gn.x), bf_lo(gn.y), bf_hi(gn.y), bf_lo(gn.z), bf_hi(gn.z), bf_lo(gn.w), bf_hi(gn.w)};
; #pragma unroll
;                         for (int e = 0; e < 8; ++e) {
;                             const float r = (1.0f + __builtin_amdgcn_exp2f(-1.4426950408889634f * ed[e])) * __builtin_amdgcn_rcpf(1.0f + __builtin_amdgcn_exp2f(-1.4426950408889634f * en[e]));
;                             acc[ai][bj][m][e >> 2][e & 3] *= r; }
.LBB0_625:
	v_pk_add_f32 v[8:9], v[160:161], 1.0 op_sel_hi:[1,0]
	v_pk_add_f32 v[158:159], v[158:159], 1.0 op_sel_hi:[1,0]
	v_pk_add_f32 v[156:157], v[156:157], 1.0 op_sel_hi:[1,0]
	v_pk_add_f32 v[6:7], v[6:7], 1.0 op_sel_hi:[1,0]
	s_waitcnt vmcnt(8)
	v_mov_b64_e32 v[182:183], v[206:207]
	v_mov_b64_e32 v[184:185], v[208:209]
	v_lshlrev_b32_e32 v5, 16, v182
	v_and_b32_e32 v160, 0xffff0000, v182
	v_lshlrev_b32_e32 v161, 16, v183
	v_and_b32_e32 v162, 0xffff0000, v183
	v_lshlrev_b32_e32 v163, 16, v184
	v_and_b32_e32 v181, 0xffff0000, v184
	v_lshlrev_b32_e32 v182, 16, v185
	v_and_b32_e32 v183, 0xffff0000, v185
	v_mul_f32_e32 v5, 0xbfb8aa3b, v5
	v_mul_f32_e32 v160, 0xbfb8aa3b, v160
	v_mul_f32_e32 v161, 0xbfb8aa3b, v161
	v_mul_f32_e32 v162, 0xbfb8aa3b, v162
	v_mul_f32_e32 v163, 0xbfb8aa3b, v163
	v_mul_f32_e32 v181, 0xbfb8aa3b, v181
	v_mul_f32_e32 v182, 0xbfb8aa3b, v182
	v_mul_f32_e32 v183, 0xbfb8aa3b, v183
	v_exp_f32_e32 v5, v5
	v_exp_f32_e32 v160, v160
	v_exp_f32_e32 v161, v161
	v_exp_f32_e32 v162, v162
	v_exp_f32_e32 v163, v163
	v_exp_f32_e32 v181, v181
	v_exp_f32_e32 v182, v182
	v_exp_f32_e32 v183, v183
	v_add_f32_e32 v5, 1.0, v5
	v_add_f32_e32 v184, 1.0, v160
	v_add_f32_e32 v185, 1.0, v161
	v_add_f32_e32 v186, 1.0, v162
	v_add_f32_e32 v187, 1.0, v163
	v_add_f32_e32 v181, 1.0, v181
	v_add_f32_e32 v188, 1.0, v182
	v_add_f32_e32 v189, 1.0, v183
	v_rcp_f32_e32 v160, v5
	v_rcp_f32_e32 v161, v184
	v_rcp_f32_e32 v162, v185
	v_rcp_f32_e32 v163, v186
	v_rcp_f32_e32 v182, v187
	v_rcp_f32_e32 v183, v181
	v_rcp_f32_e32 v184, v188
	v_rcp_f32_e32 v185, v189
	v_pk_mul_f32 v[158:159], v[158:159], v[160:161]
	v_pk_mul_f32 v[8:9], v[8:9], v[162:163]
	v_pk_mul_f32 v[6:7], v[6:7], v[182:183]
	v_pk_mul_f32 v[156:157], v[156:157], v[184:185]
	v_pk_mul_f32 v[104:105], v[104:105], v[8:9]
	v_pk_mul_f32 v[102:103], v[102:103], v[158:159]
	v_pk_mul_f32 v[100:101], v[100:101], v[156:157]
	v_pk_mul_f32 v[98:99], v[98:99], v[6:7]
	s_and_b64 vcc, exec, s[4:5]
	s_cbranch_vccz .LBB0_568
	s_branch .LBB0_569

; __device__ __forceinline__ float bf_lo(unsigned w) { return __uint_as_float(w << 16); }
; __device__ __forceinline__ float bf_hi(unsigned w) { return __uint_as_float(w & 0xffff0000u); }
;     __device__ __forceinline__ void operator()(f32x4 (&acc)[2][2][4][2], const Unit& u, int wr, int wc, int fr, int fq) const {
;     ...
;                     if (u.tag == 0) {
;                         const u32x4 gn = *(const u32x4*)(GNA + ro + bj * 32);
;                         const float en[8] = {bf_lo(gn.x), bf_hi(gn.x), bf_lo(gn.y), bf_hi(gn.y), bf_lo(gn.z), bf_hi(gn.z), bf_lo(gn.w), bf_hi(gn.w)};
; #pragma unroll
;                         for (int e = 0; e < 8; ++e) {
;                             const float r = (1.0f + __builtin_amdgcn_exp2f(-1.4426950408889634f * ed[e])) * __builtin_amdgcn_rcpf(1.0f + __builtin_amdgcn_exp2f(-1.4426950408889634f * en[e]));
;                             acc[ai][bj][m][e >> 2][e & 3] *= r; }
.LBB0_627:
	v_pk_add_f32 v[6:7], v[160:161], 1.0 op_sel_hi:[1,0]
	v_pk_add_f32 v[158:159], v[158:159], 1.0 op_sel_hi:[1,0]
	v_pk_add_f32 v[156:157], v[156:157], 1.0 op_sel_hi:[1,0]
	v_pk_add_f32 v[8:9], v[8:9], 1.0 op_sel_hi:[1,0]
	s_waitcnt vmcnt(8)
	v_mov_b64_e32 v[182:183], v[222:223]
	v_mov_b64_e32 v[184:185], v[224:225]
	v_lshlrev_b32_e32 v5, 16, v182
	v_and_b32_e32 v160, 0xffff0000, v182
	v_lshlrev_b32_e32 v161, 16, v183
	v_and_b32_e32 v162, 0xffff0000, v183
	v_lshlrev_b32_e32 v163, 16, v184
	v_and_b32_e32 v181, 0xffff0000, v184
	v_lshlrev_b32_e32 v182, 16, v185
	v_and_b32_e32 v183, 0xffff0000, v185
	v_mul_f32_e32 v5, 0xbfb8aa3b, v5
	v_mul_f32_e32 v160, 0xbfb8aa3b, v160
	v_mul_f32_e32 v161, 0xbfb8aa3b, v161
	v_mul_f32_e32 v162, 0xbfb8aa3b, v162
	v_mul_f32_e32 v163, 0xbfb8aa3b, v163
	v_mul_f32_e32 v181, 0xbfb8aa3b, v181
	v_mul_f32_e32 v182, 0xbfb8aa3b, v182
	v_mul_f32_e32 v183, 0xbfb8aa3b, v183
	v_exp_f32_e32 v5, v5
	v_exp_f32_e32 v160, v160
	v_exp_f32_e32 v161, v161
	v_exp_f32_e32 v162, v162
	v_exp_f32_e32 v163, v163
	v_exp_f32_e32 v181, v181
	v_exp_f32_e32 v182, v182
	v_exp_f32_e32 v183, v183
	v_add_f32_e32 v5, 1.0, v5
	v_add_f32_e32 v184, 1.0, v160
	v_add_f32_e32 v185, 1.0, v161
	v_add_f32_e32 v186, 1.0, v162
	v_add_f32_e32 v187, 1.0, v163
	v_add_f32_e32 v181, 1.0, v181
	v_add_f32_e32 v188, 1.0, v182
	v_add_f32_e32 v189, 1.0, v183
	v_rcp_f32_e32 v160, v5
	v_rcp_f32_e32 v161, v184
	v_rcp_f32_e32 v162, v185
	v_rcp_f32_e32 v163, v186
	v_rcp_f32_e32 v182, v187
	v_rcp_f32_e32 v183, v181
	v_rcp_f32_e32 v184, v188
	v_rcp_f32_e32 v185, v189
	v_pk_mul_f32 v[158:159], v[158:159], v[160:161]
	v_pk_mul_f32 v[6:7], v[6:7], v[162:163]
	v_pk_mul_f32 v[8:9], v[8:9], v[182:183]
	v_pk_mul_f32 v[156:157], v[156:157], v[184:185]
	v_pk_mul_f32 v[96:97], v[96:97], v[6:7]
	v_pk_mul_f32 v[94:95], v[94:95], v[158:159]
	v_pk_mul_f32 v[92:93], v[92:93], v[156:157]
	v_pk_mul_f32 v[90:91], v[90:91], v[8:9]
	s_and_b64 vcc, exec, s[4:5]
	s_cbranch_vccz .LBB0_576
	s_branch .LBB0_577

; __device__ __forceinline__ float bf_lo(unsigned w) { return __uint_as_float(w << 16); }
; __device__ __forceinline__ float bf_hi(unsigned w) { return __uint_as_float(w & 0xffff0000u); }
;     __device__ __forceinline__ void operator()(f32x4 (&acc)[2][2][4][2], const Unit& u, int wr, int wc, int fr, int fq) const {
;     ...
;                     if (u.tag == 0) {
;                         const u32x4 gn = *(const u32x4*)(GNA + ro + bj * 32);
;                         const float en[8] = {bf_lo(gn.x), bf_hi(gn.x), bf_lo(gn.y), bf_hi(gn.y), bf_lo(gn.z), bf_hi(gn.z), bf_lo(gn.w), bf_hi(gn.w)};
; #pragma unroll
;                         for (int e = 0; e < 8; ++e) {
;                             const float r = (1.0f + __builtin_amdgcn_exp2f(-1.4426950408889634f * ed[e])) * __builtin_amdgcn_rcpf(1.0f + __builtin_amdgcn_exp2f(-1.4426950408889634f * en[e]));
;                             acc[ai][bj][m][e >> 2][e & 3] *= r; }
.LBB0_629:
	v_pk_add_f32 v[6:7], v[160:161], 1.0 op_sel_hi:[1,0]
	v_pk_add_f32 v[158:159], v[158:159], 1.0 op_sel_hi:[1,0]
	v_pk_add_f32 v[156:157], v[156:157], 1.0 op_sel_hi:[1,0]
	v_pk_add_f32 v[8:9], v[8:9], 1.0 op_sel_hi:[1,0]
	s_waitcnt vmcnt(8)
	v_mov_b64_e32 v[182:183], v[238:239]
	v_mov_b64_e32 v[184:185], v[240:241]
	v_lshlrev_b32_e32 v5, 16, v182
	v_and_b32_e32 v160, 0xffff0000, v182
	v_lshlrev_b32_e32 v161, 16, v183
	v_and_b32_e32 v162, 0xffff0000, v183
	v_lshlrev_b32_e32 v163, 16, v184
	v_and_b32_e32 v181, 0xffff0000, v184
	v_lshlrev_b32_e32 v182, 16, v185
	v_and_b32_e32 v183, 0xffff0000, v185
	v_mul_f32_e32 v5, 0xbfb8aa3b, v5
	v_mul_f32_e32 v160, 0xbfb8aa3b, v160
	v_mul_f32_e32 v161, 0xbfb8aa3b, v161
	v_mul_f32_e32 v162, 0xbfb8aa3b, v162
	v_mul_f32_e32 v163, 0xbfb8aa3b, v163
	v_mul_f32_e32 v181, 0xbfb8aa3b, v181
	v_mul_f32_e32 v182, 0xbfb8aa3b, v182
	v_mul_f32_e32 v183, 0xbfb8aa3b, v183
	v_exp_f32_e32 v5, v5
	v_exp_f32_e32 v160, v160
	v_exp_f32_e32 v161, v161
	v_exp_f32_e32 v162, v162
	v_exp_f32_e32 v163, v163
	v_exp_f32_e32 v181, v181
	v_exp_f32_e32 v182, v182
	v_exp_f32_e32 v183, v183
	v_add_f32_e32 v5, 1.0, v5
	v_add_f32_e32 v184, 1.0, v160
	v_add_f32_e32 v185, 1.0, v161
	v_add_f32_e32 v186, 1.0, v162
	v_add_f32_e32 v187, 1.0, v163
	v_add_f32_e32 v181, 1.0, v181
	v_add_f32_e32 v188, 1.0, v182
	v_add_f32_e32 v189, 1.0, v183
	v_rcp_f32_e32 v160, v5
	v_rcp_f32_e32 v161, v184
	v_rcp_f32_e32 v162, v185
	v_rcp_f32_e32 v163, v186
	v_rcp_f32_e32 v182, v187
	v_rcp_f32_e32 v183, v181
	v_rcp_f32_e32 v184, v188
	v_rcp_f32_e32 v185, v189
	v_pk_mul_f32 v[158:159], v[158:159], v[160:161]
	v_pk_mul_f32 v[6:7], v[6:7], v[162:163]
	v_pk_mul_f32 v[8:9], v[8:9], v[182:183]
	v_pk_mul_f32 v[156:157], v[156:157], v[184:185]
	v_pk_mul_f32 v[88:89], v[88:89], v[6:7]
	v_pk_mul_f32 v[86:87], v[86:87], v[158:159]
	v_pk_mul_f32 v[84:85], v[84:85], v[156:157]
	v_pk_mul_f32 v[82:83], v[82:83], v[8:9]
	s_and_b64 vcc, exec, s[4:5]
	s_cbranch_vccz .LBB0_584
	s_branch .LBB0_585

; __device__ __forceinline__ float bf_lo(unsigned w) { return __uint_as_float(w << 16); }
; __device__ __forceinline__ float bf_hi(unsigned w) { return __uint_as_float(w & 0xffff0000u); }
;     __device__ __forceinline__ void operator()(f32x4 (&acc)[2][2][4][2], const Unit& u, int wr, int wc, int fr, int fq) const {
;     ...
;                     if (u.tag == 0) {
;                         const u32x4 gn = *(const u32x4*)(GNA + ro + bj * 32);
;                         const float en[8] = {bf_lo(gn.x), bf_hi(gn.x), bf_lo(gn.y), bf_hi(gn.y), bf_lo(gn.z), bf_hi(gn.z), bf_lo(gn.w), bf_hi(gn.w)};
; #pragma unroll
;                         for (int e = 0; e < 8; ++e) {
;                             const float r = (1.0f + __builtin_amdgcn_exp2f(-1.4426950408889634f * ed[e])) * __builtin_amdgcn_rcpf(1.0f + __builtin_amdgcn_exp2f(-1.4426950408889634f * en[e]));
;                             acc[ai][bj][m][e >> 2][e & 3] *= r; }
.LBB0_631:
	v_pk_add_f32 v[6:7], v[160:161], 1.0 op_sel_hi:[1,0]
	v_pk_add_f32 v[158:159], v[158:159], 1.0 op_sel_hi:[1,0]
	v_pk_add_f32 v[156:157], v[156:157], 1.0 op_sel_hi:[1,0]
	v_pk_add_f32 v[8:9], v[8:9], 1.0 op_sel_hi:[1,0]
	s_waitcnt vmcnt(8)
	v_mov_b64_e32 v[182:183], v[206:207]
	v_mov_b64_e32 v[184:185], v[208:209]
	v_lshlrev_b32_e32 v5, 16, v182
	v_and_b32_e32 v160, 0xffff0000, v182
	v_lshlrev_b32_e32 v161, 16, v183
	v_and_b32_e32 v162, 0xffff0000, v183
	v_lshlrev_b32_e32 v163, 16, v184
	v_and_b32_e32 v181, 0xffff0000, v184
	v_lshlrev_b32_e32 v182, 16, v185
	v_and_b32_e32 v183, 0xffff0000, v185
	v_mul_f32_e32 v5, 0xbfb8aa3b, v5
	v_mul_f32_e32 v160, 0xbfb8aa3b, v160
	v_mul_f32_e32 v161, 0xbfb8aa3b, v161
	v_mul_f32_e32 v162, 0xbfb8aa3b, v162
	v_mul_f32_e32 v163, 0xbfb8aa3b, v163
	v_mul_f32_e32 v181, 0xbfb8aa3b, v181
	v_mul_f32_e32 v182, 0xbfb8aa3b, v182
	v_mul_f32_e32 v183, 0xbfb8aa3b, v183
	v_exp_f32_e32 v5, v5
	v_exp_f32_e32 v160, v160
	v_exp_f32_e32 v161, v161
	v_exp_f32_e32 v162, v162
	v_exp_f32_e32 v163, v163
	v_exp_f32_e32 v181, v181
	v_exp_f32_e32 v182, v182
	v_exp_f32_e32 v183, v183
	v_add_f32_e32 v5, 1.0, v5
	v_add_f32_e32 v184, 1.0, v160
	v_add_f32_e32 v185, 1.0, v161
	v_add_f32_e32 v186, 1.0, v162
	v_add_f32_e32 v187, 1.0, v163
	v_add_f32_e32 v181, 1.0, v181
	v_add_f32_e32 v188, 1.0, v182
	v_add_f32_e32 v189, 1.0, v183
	v_rcp_f32_e32 v160, v5
	v_rcp_f32_e32 v161, v184
	v_rcp_f32_e32 v162, v185
	v_rcp_f32_e32 v163, v186
	v_rcp_f32_e32 v182, v187
	v_rcp_f32_e32 v183, v181
	v_rcp_f32_e32 v184, v188
	v_rcp_f32_e32 v185, v189
	v_pk_mul_f32 v[158:159], v[158:159], v[160:161]
	v_pk_mul_f32 v[6:7], v[6:7], v[162:163]
	v_pk_mul_f32 v[8:9], v[8:9], v[182:183]
	v_pk_mul_f32 v[156:157], v[156:157], v[184:185]
	v_pk_mul_f32 v[80:81], v[80:81], v[6:7]
	v_pk_mul_f32 v[78:79], v[78:79], v[158:159]
	v_pk_mul_f32 v[76:77], v[76:77], v[156:157]
	v_pk_mul_f32 v[74:75], v[74:75], v[8:9]
	s_and_b64 vcc, exec, s[4:5]
	s_cbranch_vccz .LBB0_592
	s_branch .LBB0_593

; __device__ __forceinline__ float bf_lo(unsigned w) { return __uint_as_float(w << 16); }
; __device__ __forceinline__ float bf_hi(unsigned w) { return __uint_as_float(w & 0xffff0000u); }
;     __device__ __forceinline__ void operator()(f32x4 (&acc)[2][2][4][2], const Unit& u, int wr, int wc, int fr, int fq) const {
;     ...
;                     if (u.tag == 0) {
;                         const u32x4 gn = *(const u32x4*)(GNA + ro + bj * 32);
;                         const float en[8] = {bf_lo(gn.x), bf_hi(gn.x), bf_lo(gn.y), bf_hi(gn.y), bf_lo(gn.z), bf_hi(gn.z), bf_lo(gn.w), bf_hi(gn.w)};
; #pragma unroll
;                         for (int e = 0; e < 8; ++e) {
;                             const float r = (1.0f + __builtin_amdgcn_exp2f(-1.4426950408889634f * ed[e])) * __builtin_amdgcn_rcpf(1.0f + __builtin_amdgcn_exp2f(-1.4426950408889634f * en[e]));
;                             acc[ai][bj][m][e >> 2][e & 3] *= r; }
.LBB0_633:
	v_pk_add_f32 v[6:7], v[160:161], 1.0 op_sel_hi:[1,0]
	v_pk_add_f32 v[158:159], v[158:159], 1.0 op_sel_hi:[1,0]
	v_pk_add_f32 v[156:157], v[156:157], 1.0 op_sel_hi:[1,0]
	v_pk_add_f32 v[8:9], v[8:9], 1.0 op_sel_hi:[1,0]
	s_waitcnt vmcnt(8)
	v_mov_b64_e32 v[182:183], v[222:223]
	v_mov_b64_e32 v[184:185], v[224:225]
	v_lshlrev_b32_e32 v5, 16, v182
	v_and_b32_e32 v160, 0xffff0000, v182
	v_lshlrev_b32_e32 v161, 16, v183
	v_and_b32_e32 v162, 0xffff0000, v183
	v_lshlrev_b32_e32 v163, 16, v184
	v_and_b32_e32 v181, 0xffff0000, v184
	v_lshlrev_b32_e32 v182, 16, v185
	v_and_b32_e32 v183, 0xffff0000, v185
	v_mul_f32_e32 v5, 0xbfb8aa3b, v5
	v_mul_f32_e32 v160, 0xbfb8aa3b, v160
	v_mul_f32_e32 v161, 0xbfb8aa3b, v161
	v_mul_f32_e32 v162, 0xbfb8aa3b, v162
	v_mul_f32_e32 v163, 0xbfb8aa3b, v163
	v_mul_f32_e32 v181, 0xbfb8aa3b, v181
	v_mul_f32_e32 v182, 0xbfb8aa3b, v182
	v_mul_f32_e32 v183, 0xbfb8aa3b, v183
	v_exp_f32_e32 v5, v5
	v_exp_f32_e32 v160, v160
	v_exp_f32_e32 v161, v161
	v_exp_f32_e32 v162, v162
	v_exp_f32_e32 v163, v163
	v_exp_f32_e32 v181, v181
	v_exp_f32_e32 v182, v182
	v_exp_f32_e32 v183, v183
	v_add_f32_e32 v5, 1.0, v5
	v_add_f32_e32 v184, 1.0, v160
	v_add_f32_e32 v185, 1.0, v161
	v_add_f32_e32 v186, 1.0, v162
	v_add_f32_e32 v187, 1.0, v163
	v_add_f32_e32 v181, 1.0, v181
	v_add_f32_e32 v188, 1.0, v182
	v_add_f32_e32 v189, 1.0, v183
	v_rcp_f32_e32 v160, v5
	v_rcp_f32_e32 v161, v184
	v_rcp_f32_e32 v162, v185
	v_rcp_f32_e32 v163, v186
	v_rcp_f32_e32 v182, v187
	v_rcp_f32_e32 v183, v181
	v_rcp_f32_e32 v184, v188
	v_rcp_f32_e32 v185, v189
	v_pk_mul_f32 v[158:159], v[158:159], v[160:161]
	v_pk_mul_f32 v[6:7], v[6:7], v[162:163]
	v_pk_mul_f32 v[8:9], v[8:9], v[182:183]
	v_pk_mul_f32 v[156:157], v[156:157], v[184:185]
	v_pk_mul_f32 v[40:41], v[40:41], v[6:7]
	v_pk_mul_f32 v[38:39], v[38:39], v[158:159]
	v_pk_mul_f32 v[36:37], v[36:37], v[156:157]
	v_pk_mul_f32 v[34:35], v[34:35], v[8:9]
	s_and_b64 vcc, exec, s[4:5]
	s_cbranch_vccz .LBB0_600
	s_branch .LBB0_601

; __device__ __forceinline__ float bf_lo(unsigned w) { return __uint_as_float(w << 16); }
; __device__ __forceinline__ float bf_hi(unsigned w) { return __uint_as_float(w & 0xffff0000u); }
;     __device__ __forceinline__ void operator()(f32x4 (&acc)[2][2][4][2], const Unit& u, int wr, int wc, int fr, int fq) const {
;     ...
;                     if (u.tag == 0) {
;                         const u32x4 gn = *(const u32x4*)(GNA + ro + bj * 32);
;                         const float en[8] = {bf_lo(gn.x), bf_hi(gn.x), bf_lo(gn.y), bf_hi(gn.y), bf_lo(gn.z), bf_hi(gn.z), bf_lo(gn.w), bf_hi(gn.w)};
; #pragma unroll
;                         for (int e = 0; e < 8; ++e) {
;                             const float r = (1.0f + __builtin_amdgcn_exp2f(-1.4426950408889634f * ed[e])) * __builtin_amdgcn_rcpf(1.0f + __builtin_amdgcn_exp2f(-1.4426950408889634f * en[e]));
;                             acc[ai][bj][m][e >> 2][e & 3] *= r; }
.LBB0_635:
	v_pk_add_f32 v[6:7], v[160:161], 1.0 op_sel_hi:[1,0]
	v_pk_add_f32 v[158:159], v[158:159], 1.0 op_sel_hi:[1,0]
	v_pk_add_f32 v[156:157], v[156:157], 1.0 op_sel_hi:[1,0]
	v_pk_add_f32 v[8:9], v[8:9], 1.0 op_sel_hi:[1,0]
	s_waitcnt vmcnt(8)
	v_mov_b64_e32 v[182:183], v[238:239]
	v_mov_b64_e32 v[184:185], v[240:241]
	v_lshlrev_b32_e32 v5, 16, v182
	v_and_b32_e32 v160, 0xffff0000, v182
	v_lshlrev_b32_e32 v161, 16, v183
	v_and_b32_e32 v162, 0xffff0000, v183
	v_lshlrev_b32_e32 v163, 16, v184
	v_and_b32_e32 v181, 0xffff0000, v184
	v_lshlrev_b32_e32 v182, 16, v185
	v_and_b32_e32 v183, 0xffff0000, v185
	v_mul_f32_e32 v5, 0xbfb8aa3b, v5
	v_mul_f32_e32 v160, 0xbfb8aa3b, v160
	v_mul_f32_e32 v161, 0xbfb8aa3b, v161
	v_mul_f32_e32 v162, 0xbfb8aa3b, v162
	v_mul_f32_e32 v163, 0xbfb8aa3b, v163
	v_mul_f32_e32 v181, 0xbfb8aa3b, v181
	v_mul_f32_e32 v182, 0xbfb8aa3b, v182
	v_mul_f32_e32 v183, 0xbfb8aa3b, v183
	v_exp_f32_e32 v5, v5
	v_exp_f32_e32 v160, v160
	v_exp_f32_e32 v161, v161
	v_exp_f32_e32 v162, v162
	v_exp_f32_e32 v163, v163
	v_exp_f32_e32 v181, v181
	v_exp_f32_e32 v182, v182
	v_exp_f32_e32 v183, v183
	v_add_f32_e32 v5, 1.0, v5
	v_add_f32_e32 v184, 1.0, v160
	v_add_f32_e32 v185, 1.0, v161
	v_add_f32_e32 v186, 1.0, v162
	v_add_f32_e32 v187, 1.0, v163
	v_add_f32_e32 v181, 1.0, v181
	v_add_f32_e32 v188, 1.0, v182
	v_add_f32_e32 v189, 1.0, v183
	v_rcp_f32_e32 v160, v5
	v_rcp_f32_e32 v161, v184
	v_rcp_f32_e32 v162, v185
	v_rcp_f32_e32 v163, v186
	v_rcp_f32_e32 v182, v187
	v_rcp_f32_e32 v183, v181
	v_rcp_f32_e32 v184, v188
	v_rcp_f32_e32 v185, v189
	v_pk_mul_f32 v[158:159], v[158:159], v[160:161]
	v_pk_mul_f32 v[6:7], v[6:7], v[162:163]
	v_pk_mul_f32 v[8:9], v[8:9], v[182:183]
	v_pk_mul_f32 v[156:157], v[156:157], v[184:185]
	v_pk_mul_f32 v[32:33], v[32:33], v[6:7]
	v_pk_mul_f32 v[30:31], v[30:31], v[158:159]
	v_pk_mul_f32 v[28:29], v[28:29], v[156:157]
	v_pk_mul_f32 v[26:27], v[26:27], v[8:9]
	s_and_b64 vcc, exec, s[4:5]
	s_cbranch_vccz .LBB0_608
	s_branch .LBB0_609

; __device__ __forceinline__ float bf_lo(unsigned w) { return __uint_as_float(w << 16); }
; __device__ __forceinline__ float bf_hi(unsigned w) { return __uint_as_float(w & 0xffff0000u); }
;     __device__ __forceinline__ void operator()(f32x4 (&acc)[2][2][4][2], const Unit& u, int wr, int wc, int fr, int fq) const {
;     ...
;                     if (u.tag == 0) {
;                         const u32x4 gn = *(const u32x4*)(GNA + ro + bj * 32);
;                         const float en[8] = {bf_lo(gn.x), bf_hi(gn.x), bf_lo(gn.y), bf_hi(gn.y), bf_lo(gn.z), bf_hi(gn.z), bf_lo(gn.w), bf_hi(gn.w)};
; #pragma unroll
;                         for (int e = 0; e < 8; ++e) {
;                             const float r = (1.0f + __builtin_amdgcn_exp2f(-1.4426950408889634f * ed[e])) * __builtin_amdgcn_rcpf(1.0f + __builtin_amdgcn_exp2f(-1.4426950408889634f * en[e]));
;                             acc[ai][bj][m][e >> 2][e & 3] *= r; }
.LBB0_637:
	v_pk_add_f32 v[6:7], v[160:161], 1.0 op_sel_hi:[1,0]
	v_pk_add_f32 v[158:159], v[158:159], 1.0 op_sel_hi:[1,0]
	v_pk_add_f32 v[156:157], v[156:157], 1.0 op_sel_hi:[1,0]
	v_pk_add_f32 v[8:9], v[8:9], 1.0 op_sel_hi:[1,0]
	s_waitcnt vmcnt(4)
	v_mov_b64_e32 v[182:183], v[206:207]
	v_mov_b64_e32 v[184:185], v[208:209]
	v_lshlrev_b32_e32 v5, 16, v182
	v_and_b32_e32 v160, 0xffff0000, v182
	v_lshlrev_b32_e32 v161, 16, v183
	v_and_b32_e32 v162, 0xffff0000, v183
	v_lshlrev_b32_e32 v163, 16, v184
	v_and_b32_e32 v181, 0xffff0000, v184
	v_lshlrev_b32_e32 v182, 16, v185
	v_and_b32_e32 v183, 0xffff0000, v185
	v_mul_f32_e32 v5, 0xbfb8aa3b, v5
	v_mul_f32_e32 v160, 0xbfb8aa3b, v160
	v_mul_f32_e32 v161, 0xbfb8aa3b, v161
	v_mul_f32_e32 v162, 0xbfb8aa3b, v162
	v_mul_f32_e32 v163, 0xbfb8aa3b, v163
	v_mul_f32_e32 v181, 0xbfb8aa3b, v181
	v_mul_f32_e32 v182, 0xbfb8aa3b, v182
	v_mul_f32_e32 v183, 0xbfb8aa3b, v183
	v_exp_f32_e32 v5, v5
	v_exp_f32_e32 v160, v160
	v_exp_f32_e32 v161, v161
	v_exp_f32_e32 v162, v162
	v_exp_f32_e32 v163, v163
	v_exp_f32_e32 v181, v181
	v_exp_f32_e32 v182, v182
	v_exp_f32_e32 v183, v183
	v_add_f32_e32 v5, 1.0, v5
	v_add_f32_e32 v184, 1.0, v160
	v_add_f32_e32 v185, 1.0, v161
	v_add_f32_e32 v186, 1.0, v162
	v_add_f32_e32 v187, 1.0, v163
	v_add_f32_e32 v181, 1.0, v181
	v_add_f32_e32 v188, 1.0, v182
	v_add_f32_e32 v189, 1.0, v183
	v_rcp_f32_e32 v160, v5
	v_rcp_f32_e32 v161, v184
	v_rcp_f32_e32 v162, v185
	v_rcp_f32_e32 v163, v186
	v_rcp_f32_e32 v182, v187
	v_rcp_f32_e32 v183, v181
	v_rcp_f32_e32 v184, v188
	v_rcp_f32_e32 v185, v189
	v_pk_mul_f32 v[158:159], v[158:159], v[160:161]
	v_pk_mul_f32 v[6:7], v[6:7], v[162:163]
	v_pk_mul_f32 v[8:9], v[8:9], v[182:183]
	v_pk_mul_f32 v[156:157], v[156:157], v[184:185]
	v_pk_mul_f32 v[24:25], v[24:25], v[6:7]
	v_pk_mul_f32 v[22:23], v[22:23], v[158:159]
	v_pk_mul_f32 v[20:21], v[20:21], v[156:157]
	v_pk_mul_f32 v[18:19], v[18:19], v[8:9]
	s_and_b64 vcc, exec, s[4:5]
	s_cbranch_vccz .LBB0_616
	s_branch .LBB0_617

; __device__ __forceinline__ float bf_lo(unsigned w) { return __uint_as_float(w << 16); }
; __device__ __forceinline__ float bf_hi(unsigned w) { return __uint_as_float(w & 0xffff0000u); }
;     __device__ __forceinline__ void operator()(f32x4 (&acc)[2][2][4][2], const Unit& u, int wr, int wc, int fr, int fq) const {
;     ...
;                     if (u.tag == 0) {
;                         const u32x4 gn = *(const u32x4*)(GNA + ro + bj * 32);
;                         const float en[8] = {bf_lo(gn.x), bf_hi(gn.x), bf_lo(gn.y), bf_hi(gn.y), bf_lo(gn.z), bf_hi(gn.z), bf_lo(gn.w), bf_hi(gn.w)};
; #pragma unroll
;                         for (int e = 0; e < 8; ++e) {
;                             const float r = (1.0f + __builtin_amdgcn_exp2f(-1.4426950408889634f * ed[e])) * __builtin_amdgcn_rcpf(1.0f + __builtin_amdgcn_exp2f(-1.4426950408889634f * en[e]));
;                             acc[ai][bj][m][e >> 2][e & 3] *= r; }
.LBB0_639:
	v_pk_add_f32 v[2:3], v[156:157], 1.0 op_sel_hi:[1,0]
	v_pk_add_f32 v[8:9], v[8:9], 1.0 op_sel_hi:[1,0]
	v_pk_add_f32 v[6:7], v[6:7], 1.0 op_sel_hi:[1,0]
	v_pk_add_f32 v[4:5], v[4:5], 1.0 op_sel_hi:[1,0]
	s_waitcnt vmcnt(0)
	v_mov_b64_e32 v[158:159], v[222:223]
	v_mov_b64_e32 v[160:161], v[224:225]
	v_lshlrev_b32_e32 v156, 16, v158
	v_and_b32_e32 v157, 0xffff0000, v158
	v_lshlrev_b32_e32 v158, 16, v159
	v_and_b32_e32 v159, 0xffff0000, v159
	v_lshlrev_b32_e32 v162, 16, v160
	v_and_b32_e32 v160, 0xffff0000, v160
	v_lshlrev_b32_e32 v163, 16, v161
	v_and_b32_e32 v161, 0xffff0000, v161
	v_mul_f32_e32 v156, 0xbfb8aa3b, v156
	v_mul_f32_e32 v157, 0xbfb8aa3b, v157
	v_mul_f32_e32 v158, 0xbfb8aa3b, v158
	v_mul_f32_e32 v159, 0xbfb8aa3b, v159
	v_mul_f32_e32 v162, 0xbfb8aa3b, v162
	v_mul_f32_e32 v160, 0xbfb8aa3b, v160
	v_mul_f32_e32 v163, 0xbfb8aa3b, v163
	v_mul_f32_e32 v161, 0xbfb8aa3b, v161
	v_exp_f32_e32 v156, v156
	v_exp_f32_e32 v157, v157
	v_exp_f32_e32 v158, v158
	v_exp_f32_e32 v159, v159
	v_exp_f32_e32 v162, v162
	v_exp_f32_e32 v160, v160
	v_exp_f32_e32 v163, v163
	v_exp_f32_e32 v161, v161
	v_add_f32_e32 v156, 1.0, v156
	v_add_f32_e32 v157, 1.0, v157
	v_add_f32_e32 v158, 1.0, v158
	v_add_f32_e32 v159, 1.0, v159
	v_add_f32_e32 v162, 1.0, v162
	v_add_f32_e32 v181, 1.0, v160
	v_add_f32_e32 v163, 1.0, v163
	v_add_f32_e32 v182, 1.0, v161
	v_rcp_f32_e32 v156, v156
	v_rcp_f32_e32 v157, v157
	v_rcp_f32_e32 v158, v158
	v_rcp_f32_e32 v159, v159
	v_rcp_f32_e32 v160, v162
	v_rcp_f32_e32 v161, v181
	v_rcp_f32_e32 v162, v163
	v_rcp_f32_e32 v163, v182
	v_pk_mul_f32 v[8:9], v[8:9], v[156:157]
	v_pk_mul_f32 v[2:3], v[2:3], v[158:159]
	v_pk_mul_f32 v[4:5], v[4:5], v[160:161]
	v_pk_mul_f32 v[6:7], v[6:7], v[162:163]
	v_pk_mul_f32 v[16:17], v[16:17], v[2:3]
	v_pk_mul_f32 v[14:15], v[14:15], v[8:9]
	v_pk_mul_f32 v[12:13], v[12:13], v[6:7]
	v_pk_mul_f32 v[10:11], v[10:11], v[4:5]
	s_mov_b64 s[4:5], -1
	s_and_b64 vcc, exec, s[50:51]
	s_cbranch_vccz .LBB0_554
